# topk per-half top16-of-64: 60-comparator 16-sorters instead of bitonic (80), same max/bitonic merges; network checked by simulation against the old section
# baseline (speedup 1.0000x reference)
.LBB0_704:
	v_cndmask_b32_e64 v0, 0, 1, s[6:7]
	s_lshl_b32 s36, s8, 8
	v_cmp_ne_u32_e32 vcc, 1, v0
	v_lshl_add_u64 v[0:1], v[178:179], 0, s[36:37]
	global_load_dwordx4 v[44:47], v[0:1], off
	global_load_dwordx4 v[40:43], v[0:1], off offset:32
	global_load_dwordx4 v[36:39], v[0:1], off offset:64
	global_load_dwordx4 v[32:35], v[0:1], off offset:96
	global_load_dwordx4 v[28:31], v[0:1], off offset:128
	global_load_dwordx4 v[24:27], v[0:1], off offset:160
	global_load_dwordx4 v[20:23], v[0:1], off offset:192
	global_load_dwordx4 v[16:19], v[0:1], off offset:224
	v_lshl_or_b32 v180, s8, 7, v209
	v_ashrrev_i32_e32 v181, 31, v180
	v_lshlrev_b64 v[0:1], 8, v[180:181]
	v_lshl_add_u64 v[60:61], v[64:65], 0, v[0:1]
	global_load_dwordx4 v[0:3], v[60:61], off
	global_load_dwordx4 v[48:51], v[60:61], off offset:32
	global_load_dwordx4 v[52:55], v[60:61], off offset:64
	global_load_dwordx4 v[56:59], v[60:61], off offset:96
	global_load_dwordx4 v[68:71], v[60:61], off offset:128
	global_load_dwordx4 v[72:75], v[60:61], off offset:160
	global_load_dwordx4 v[76:79], v[60:61], off offset:192
	global_load_dwordx4 v[80:83], v[60:61], off offset:224
	s_mov_b32 s12, 0x2000
	s_mov_b32 s13, 0
	v_lshl_add_u64 v[186:187], v[60:61], 0, s[12:13]
	global_load_dwordx4 v[84:87], v[186:187], off
	global_load_dwordx4 v[88:91], v[186:187], off offset:32
	global_load_dwordx4 v[92:95], v[186:187], off offset:64
	global_load_dwordx4 v[96:99], v[186:187], off offset:96
	global_load_dwordx4 v[100:103], v[186:187], off offset:128
	global_load_dwordx4 v[104:107], v[186:187], off offset:160
	global_load_dwordx4 v[108:111], v[186:187], off offset:192
	global_load_dwordx4 v[112:115], v[186:187], off offset:224
	v_lshl_add_u64 v[188:189], v[186:187], 0, s[12:13]
	global_load_dwordx4 v[116:119], v[188:189], off
	global_load_dwordx4 v[120:123], v[188:189], off offset:32
	global_load_dwordx4 v[124:127], v[188:189], off offset:64
	global_load_dwordx4 v[128:131], v[188:189], off offset:96
	global_load_dwordx4 v[132:135], v[188:189], off offset:128
	global_load_dwordx4 v[136:139], v[188:189], off offset:160
	global_load_dwordx4 v[140:143], v[188:189], off offset:192
	global_load_dwordx4 v[152:155], v[188:189], off offset:224
	v_lshl_add_u64 v[186:187], v[188:189], 0, s[12:13]
	global_load_dwordx4 v[156:159], v[186:187], off
	global_load_dwordx4 v[160:163], v[186:187], off offset:32
	global_load_dwordx4 v[164:167], v[186:187], off offset:64
	global_load_dwordx4 v[168:171], v[186:187], off offset:96
	s_waitcnt vmcnt(24)
	v_mfma_f32_32x32x16_bf16 v[0:15], v[0:3], v[44:47], 0
	v_mfma_f32_32x32x16_bf16 v[0:15], v[48:51], v[40:43], v[0:15]
	v_mfma_f32_32x32x16_bf16 v[0:15], v[52:55], v[36:39], v[0:15]
	v_mfma_f32_32x32x16_bf16 v[0:15], v[56:59], v[32:35], v[0:15]
	global_load_dwordx4 v[48:51], v[186:187], off offset:128
	global_load_dwordx4 v[52:55], v[186:187], off offset:160
	global_load_dwordx4 v[56:59], v[186:187], off offset:192
	global_load_dwordx4 v[60:63], v[186:187], off offset:224
	s_waitcnt vmcnt(27)
	v_mfma_f32_32x32x16_bf16 v[0:15], v[68:71], v[28:31], v[0:15]
	s_waitcnt vmcnt(26)
	v_mfma_f32_32x32x16_bf16 v[0:15], v[72:75], v[24:27], v[0:15]
	s_waitcnt vmcnt(25)
	v_mfma_f32_32x32x16_bf16 v[0:15], v[76:79], v[20:23], v[0:15]
	s_waitcnt vmcnt(24)
	v_mfma_f32_32x32x16_bf16 v[0:15], v[80:83], v[16:19], v[0:15]
	v_or_b32_e32 v172, 1, v66
	v_xor_b32_e32 v174, 0x7e, v66
	s_nop 9
	v_cmp_gt_i32_e64 s[6:7], 0, v1
	v_xor_b32_e32 v67, 0x7f, v66
	v_and_b32_e32 v1, 0xffffff80, v1
	v_cndmask_b32_e64 v172, v174, v172, s[6:7]
	v_cmp_gt_i32_e64 s[6:7], 0, v0
	v_and_b32_e32 v0, 0xffffff80, v0
	v_or_b32_e32 v210, v172, v1
	v_cndmask_b32_e64 v67, v67, v66, s[6:7]
	v_or_b32_e32 v211, v67, v0
	v_or_b32_e32 v1, 3, v66
	v_xor_b32_e32 v173, 0x7c, v66
	v_cmp_gt_i32_e64 s[6:7], 0, v3
	v_or_b32_e32 v0, 2, v66
	v_xor_b32_e32 v190, 0x7d, v66
	v_cndmask_b32_e64 v1, v173, v1, s[6:7]
	v_cmp_gt_i32_e64 s[6:7], 0, v2
	v_and_b32_e32 v3, 0xffffff80, v3
	v_and_b32_e32 v2, 0xffffff80, v2
	v_cndmask_b32_e64 v0, v190, v0, s[6:7]
	v_or_b32_e32 v173, v1, v3
	v_or_b32_e32 v1, 9, v66
	v_xor_b32_e32 v3, 0x76, v66
	v_cmp_gt_i32_e64 s[6:7], 0, v5
	v_or_b32_e32 v212, v0, v2
	v_or_b32_e32 v0, 8, v66
	v_cndmask_b32_e64 v1, v3, v1, s[6:7]
	v_xor_b32_e32 v2, 0x77, v66
	v_cmp_gt_i32_e64 s[6:7], 0, v4
	v_and_b32_e32 v3, 0xffffff80, v4
	s_nop 0
	v_cndmask_b32_e64 v0, v2, v0, s[6:7]
	v_and_b32_e32 v2, 0xffffff80, v5
	v_or_b32_e32 v213, v1, v2
	v_or_b32_e32 v214, v0, v3
	v_or_b32_e32 v1, 11, v66
	v_xor_b32_e32 v3, 0x74, v66
	v_cmp_gt_i32_e64 s[6:7], 0, v7
	v_or_b32_e32 v0, 10, v66
	v_xor_b32_e32 v2, 0x75, v66
	v_cndmask_b32_e64 v1, v3, v1, s[6:7]
	v_cmp_gt_i32_e64 s[6:7], 0, v6
	v_and_b32_e32 v3, 0xffffff80, v6
	s_nop 0
	v_cndmask_b32_e64 v0, v2, v0, s[6:7]
	v_and_b32_e32 v2, 0xffffff80, v7
	v_or_b32_e32 v215, v1, v2
	v_or_b32_e32 v216, v0, v3
	v_or_b32_e32 v1, 17, v66
	v_xor_b32_e32 v3, 0x6e, v66
	v_cmp_gt_i32_e64 s[6:7], 0, v9
	v_or_b32_e32 v0, 16, v66
	v_xor_b32_e32 v2, 0x6f, v66
	v_cndmask_b32_e64 v1, v3, v1, s[6:7]
	v_cmp_gt_i32_e64 s[6:7], 0, v8
	v_and_b32_e32 v3, 0xffffff80, v8
	s_nop 0
	v_cndmask_b32_e64 v0, v2, v0, s[6:7]
	v_and_b32_e32 v2, 0xffffff80, v9
	v_or_b32_e32 v217, v1, v2
	v_or_b32_e32 v218, v0, v3
	v_or_b32_e32 v1, 19, v66
	v_xor_b32_e32 v3, 0x6c, v66
	v_cmp_gt_i32_e64 s[6:7], 0, v11
	v_or_b32_e32 v0, 18, v66
	v_xor_b32_e32 v2, 0x6d, v66
	v_cndmask_b32_e64 v1, v3, v1, s[6:7]
	v_cmp_gt_i32_e64 s[6:7], 0, v10
	v_and_b32_e32 v3, 0xffffff80, v10
	s_nop 0
	v_cndmask_b32_e64 v0, v2, v0, s[6:7]
	v_and_b32_e32 v2, 0xffffff80, v11
	v_or_b32_e32 v219, v1, v2
	v_or_b32_e32 v220, v0, v3
	v_or_b32_e32 v1, 25, v66
	v_xor_b32_e32 v3, 0x66, v66
	v_cmp_gt_i32_e64 s[6:7], 0, v13
	v_or_b32_e32 v0, 24, v66
	v_xor_b32_e32 v2, 0x67, v66
	v_cndmask_b32_e64 v1, v3, v1, s[6:7]
	v_cmp_gt_i32_e64 s[6:7], 0, v12
	v_and_b32_e32 v3, 0xffffff80, v12
	s_nop 0
	v_cndmask_b32_e64 v0, v2, v0, s[6:7]
	v_and_b32_e32 v2, 0xffffff80, v13
	v_or_b32_e32 v221, v1, v2
	v_or_b32_e32 v1, 27, v66
	v_cmp_gt_i32_e64 s[6:7], 0, v15
	v_or_b32_e32 v222, v0, v3
	v_and_b32_e32 v2, 0xffffff80, v15
	v_xor_b32_e32 v0, 0x64, v66
	v_cndmask_b32_e64 v0, v0, v1, s[6:7]
	v_cmp_gt_i32_e64 s[6:7], 0, v14
	v_and_b32_e32 v3, 0xffffff80, v14
	v_or_b32_e32 v223, v0, v2
	v_xor_b32_e32 v1, 0x65, v66
	v_or_b32_e32 v188, 26, v66
	v_cndmask_b32_e64 v1, v1, v188, s[6:7]
	v_or_b32_e32 v224, v1, v3
	s_waitcnt vmcnt(23)
	v_mfma_f32_32x32x16_bf16 v[0:15], v[84:87], v[44:47], 0
	s_waitcnt vmcnt(22)
	v_mfma_f32_32x32x16_bf16 v[0:15], v[88:91], v[40:43], v[0:15]
	s_waitcnt vmcnt(21)
	v_mfma_f32_32x32x16_bf16 v[0:15], v[92:95], v[36:39], v[0:15]
	s_waitcnt vmcnt(20)
	v_mfma_f32_32x32x16_bf16 v[0:15], v[96:99], v[32:35], v[0:15]
	s_waitcnt vmcnt(19)
	v_mfma_f32_32x32x16_bf16 v[0:15], v[100:103], v[28:31], v[0:15]
	s_waitcnt vmcnt(18)
	v_mfma_f32_32x32x16_bf16 v[0:15], v[104:107], v[24:27], v[0:15]
	s_waitcnt vmcnt(17)
	v_mfma_f32_32x32x16_bf16 v[0:15], v[108:111], v[20:23], v[0:15]
	s_waitcnt vmcnt(16)
	v_mfma_f32_32x32x16_bf16 v[0:15], v[112:115], v[16:19], v[0:15]
	s_nop 3
	s_nop 7
	v_cmp_gt_i32_e64 s[6:7], 0, v1
	v_and_b32_e32 v1, 0xffffff80, v1
	v_xor_b32_e32 v181, 0x5e, v66
	v_or_b32_e32 v188, 33, v66
	v_cndmask_b32_e64 v181, v181, v188, s[6:7]
	v_cmp_gt_i32_e64 s[6:7], 0, v0
	v_and_b32_e32 v0, 0xffffff80, v0
	v_or_b32_e32 v225, v181, v1
	v_xor_b32_e32 v190, 0x5f, v66
	v_or_b32_e32 v188, 32, v66
	v_cndmask_b32_e64 v190, v190, v188, s[6:7]
	v_cmp_gt_i32_e64 s[6:7], 0, v3
	v_or_b32_e32 v226, v190, v0
	v_and_b32_e32 v3, 0xffffff80, v3
	v_xor_b32_e32 v0, 0x5c, v66
	v_or_b32_e32 v188, 35, v66
	v_cndmask_b32_e64 v0, v0, v188, s[6:7]
	v_cmp_gt_i32_e64 s[6:7], 0, v2
	v_and_b32_e32 v2, 0xffffff80, v2
	v_or_b32_e32 v227, v0, v3
	v_xor_b32_e32 v1, 0x5d, v66
	v_or_b32_e32 v188, 34, v66
	v_cndmask_b32_e64 v1, v1, v188, s[6:7]
	v_cmp_gt_i32_e64 s[6:7], 0, v5
	v_or_b32_e32 v228, v1, v2
	v_and_b32_e32 v2, 0xffffff80, v5
	v_xor_b32_e32 v0, 0x56, v66
	v_or_b32_e32 v188, 41, v66
	v_cndmask_b32_e64 v0, v0, v188, s[6:7]
	v_cmp_gt_i32_e64 s[6:7], 0, v4
	v_and_b32_e32 v3, 0xffffff80, v4
	v_or_b32_e32 v229, v0, v2
	v_xor_b32_e32 v1, 0x57, v66
	v_or_b32_e32 v188, 40, v66
	v_cndmask_b32_e64 v1, v1, v188, s[6:7]
	v_cmp_gt_i32_e64 s[6:7], 0, v7
	v_or_b32_e32 v230, v1, v3
	v_and_b32_e32 v2, 0xffffff80, v7
	v_xor_b32_e32 v0, 0x54, v66
	v_or_b32_e32 v188, 43, v66
	v_cndmask_b32_e64 v0, v0, v188, s[6:7]
	v_cmp_gt_i32_e64 s[6:7], 0, v6
	v_and_b32_e32 v3, 0xffffff80, v6
	v_or_b32_e32 v231, v0, v2
	v_xor_b32_e32 v1, 0x55, v66
	v_or_b32_e32 v188, 42, v66
	v_cndmask_b32_e64 v1, v1, v188, s[6:7]
	v_cmp_gt_i32_e64 s[6:7], 0, v9
	v_or_b32_e32 v232, v1, v3
	v_and_b32_e32 v2, 0xffffff80, v9
	v_xor_b32_e32 v0, 0x4e, v66
	v_or_b32_e32 v188, 49, v66
	v_cndmask_b32_e64 v0, v0, v188, s[6:7]
	v_cmp_gt_i32_e64 s[6:7], 0, v8
	v_and_b32_e32 v3, 0xffffff80, v8
	v_or_b32_e32 v233, v0, v2
	v_xor_b32_e32 v1, 0x4f, v66
	v_or_b32_e32 v188, 48, v66
	v_cndmask_b32_e64 v1, v1, v188, s[6:7]
	v_cmp_gt_i32_e64 s[6:7], 0, v11
	v_or_b32_e32 v234, v1, v3
	v_and_b32_e32 v2, 0xffffff80, v11
	v_xor_b32_e32 v0, 0x4c, v66
	v_or_b32_e32 v188, 51, v66
	v_cndmask_b32_e64 v0, v0, v188, s[6:7]
	v_cmp_gt_i32_e64 s[6:7], 0, v10
	v_and_b32_e32 v3, 0xffffff80, v10
	v_or_b32_e32 v235, v0, v2
	v_xor_b32_e32 v1, 0x4d, v66
	v_or_b32_e32 v188, 50, v66
	v_cndmask_b32_e64 v1, v1, v188, s[6:7]
	v_cmp_gt_i32_e64 s[6:7], 0, v13
	v_or_b32_e32 v236, v1, v3
	v_and_b32_e32 v2, 0xffffff80, v13
	v_xor_b32_e32 v0, 0x46, v66
	v_or_b32_e32 v188, 57, v66
	v_cndmask_b32_e64 v0, v0, v188, s[6:7]
	v_cmp_gt_i32_e64 s[6:7], 0, v12
	v_and_b32_e32 v3, 0xffffff80, v12
	v_or_b32_e32 v237, v0, v2
	v_xor_b32_e32 v1, 0x47, v66
	v_or_b32_e32 v188, 56, v66
	v_cndmask_b32_e64 v1, v1, v188, s[6:7]
	v_cmp_gt_i32_e64 s[6:7], 0, v15
	v_or_b32_e32 v238, v1, v3
	v_and_b32_e32 v2, 0xffffff80, v15
	v_xor_b32_e32 v0, 0x44, v66
	v_or_b32_e32 v188, 59, v66
	v_cndmask_b32_e64 v0, v0, v188, s[6:7]
	v_cmp_gt_i32_e64 s[6:7], 0, v14
	v_and_b32_e32 v3, 0xffffff80, v14
	v_or_b32_e32 v239, v0, v2
	v_xor_b32_e32 v1, 0x45, v66
	v_or_b32_e32 v188, 58, v66
	v_cndmask_b32_e64 v1, v1, v188, s[6:7]
	v_or_b32_e32 v240, v1, v3
	s_waitcnt vmcnt(15)
	v_mfma_f32_32x32x16_bf16 v[0:15], v[116:119], v[44:47], 0
	s_waitcnt vmcnt(14)
	v_mfma_f32_32x32x16_bf16 v[0:15], v[120:123], v[40:43], v[0:15]
	s_waitcnt vmcnt(13)
	v_mfma_f32_32x32x16_bf16 v[0:15], v[124:127], v[36:39], v[0:15]
	s_waitcnt vmcnt(12)
	v_mfma_f32_32x32x16_bf16 v[0:15], v[128:131], v[32:35], v[0:15]
	s_waitcnt vmcnt(11)
	v_mfma_f32_32x32x16_bf16 v[0:15], v[132:135], v[28:31], v[0:15]
	s_waitcnt vmcnt(10)
	v_mfma_f32_32x32x16_bf16 v[0:15], v[136:139], v[24:27], v[0:15]
	s_waitcnt vmcnt(9)
	v_mfma_f32_32x32x16_bf16 v[0:15], v[140:143], v[20:23], v[0:15]
	s_waitcnt vmcnt(8)
	v_mfma_f32_32x32x16_bf16 v[0:15], v[152:155], v[16:19], v[0:15]
	s_nop 3
	s_nop 7
	v_cmp_gt_i32_e64 s[6:7], 0, v1
	v_and_b32_e32 v1, 0xffffff80, v1
	v_xor_b32_e32 v182, 62, v66
	v_or_b32_e32 v188, 0x41, v66
	v_cndmask_b32_e64 v182, v182, v188, s[6:7]
	v_cmp_gt_i32_e64 s[6:7], 0, v0
	v_and_b32_e32 v0, 0xffffff80, v0
	v_or_b32_e32 v182, v182, v1
	v_xor_b32_e32 v183, 63, v66
	v_or_b32_e32 v188, 64, v66
	v_cndmask_b32_e64 v183, v183, v188, s[6:7]
	v_cmp_gt_i32_e64 s[6:7], 0, v3
	v_or_b32_e32 v183, v183, v0
	v_and_b32_e32 v3, 0xffffff80, v3
	v_xor_b32_e32 v0, 60, v66
	v_or_b32_e32 v188, 0x43, v66
	v_cndmask_b32_e64 v0, v0, v188, s[6:7]
	v_cmp_gt_i32_e64 s[6:7], 0, v2
	v_and_b32_e32 v2, 0xffffff80, v2
	v_or_b32_e32 v241, v0, v3
	v_xor_b32_e32 v1, 61, v66
	v_or_b32_e32 v188, 0x42, v66
	v_cndmask_b32_e64 v1, v1, v188, s[6:7]
	v_cmp_gt_i32_e64 s[6:7], 0, v5
	v_or_b32_e32 v242, v1, v2
	v_and_b32_e32 v2, 0xffffff80, v5
	v_xor_b32_e32 v0, 54, v66
	v_or_b32_e32 v188, 0x49, v66
	v_cndmask_b32_e64 v0, v0, v188, s[6:7]
	v_cmp_gt_i32_e64 s[6:7], 0, v4
	v_and_b32_e32 v3, 0xffffff80, v4
	v_or_b32_e32 v243, v0, v2
	v_xor_b32_e32 v1, 55, v66
	v_or_b32_e32 v188, 0x48, v66
	v_cndmask_b32_e64 v1, v1, v188, s[6:7]
	v_cmp_gt_i32_e64 s[6:7], 0, v7
	v_or_b32_e32 v244, v1, v3
	v_and_b32_e32 v2, 0xffffff80, v7
	v_xor_b32_e32 v0, 52, v66
	v_or_b32_e32 v188, 0x4b, v66
	v_cndmask_b32_e64 v0, v0, v188, s[6:7]
	v_cmp_gt_i32_e64 s[6:7], 0, v6
	v_and_b32_e32 v3, 0xffffff80, v6
	v_or_b32_e32 v245, v0, v2
	v_xor_b32_e32 v1, 53, v66
	v_or_b32_e32 v188, 0x4a, v66
	v_cndmask_b32_e64 v1, v1, v188, s[6:7]
	v_cmp_gt_i32_e64 s[6:7], 0, v9
	v_or_b32_e32 v246, v1, v3
	v_and_b32_e32 v2, 0xffffff80, v9
	v_xor_b32_e32 v0, 46, v66
	v_or_b32_e32 v188, 0x51, v66
	v_cndmask_b32_e64 v0, v0, v188, s[6:7]
	v_cmp_gt_i32_e64 s[6:7], 0, v8
	v_and_b32_e32 v3, 0xffffff80, v8
	v_or_b32_e32 v247, v0, v2
	v_xor_b32_e32 v1, 47, v66
	v_or_b32_e32 v188, 0x50, v66
	v_cndmask_b32_e64 v1, v1, v188, s[6:7]
	v_cmp_gt_i32_e64 s[6:7], 0, v11
	v_or_b32_e32 v248, v1, v3
	v_and_b32_e32 v2, 0xffffff80, v11
	v_xor_b32_e32 v0, 44, v66
	v_or_b32_e32 v188, 0x53, v66
	v_cndmask_b32_e64 v0, v0, v188, s[6:7]
	v_cmp_gt_i32_e64 s[6:7], 0, v10
	v_and_b32_e32 v3, 0xffffff80, v10
	v_or_b32_e32 v249, v0, v2
	v_xor_b32_e32 v1, 45, v66
	v_or_b32_e32 v188, 0x52, v66
	v_cndmask_b32_e64 v1, v1, v188, s[6:7]
	v_cmp_gt_i32_e64 s[6:7], 0, v13
	v_or_b32_e32 v250, v1, v3
	v_and_b32_e32 v2, 0xffffff80, v13
	v_xor_b32_e32 v0, 38, v66
	v_or_b32_e32 v188, 0x59, v66
	v_cndmask_b32_e64 v0, v0, v188, s[6:7]
	v_cmp_gt_i32_e64 s[6:7], 0, v12
	v_and_b32_e32 v3, 0xffffff80, v12
	v_or_b32_e32 v251, v0, v2
	v_xor_b32_e32 v1, 39, v66
	v_or_b32_e32 v188, 0x58, v66
	v_cndmask_b32_e64 v1, v1, v188, s[6:7]
	v_cmp_gt_i32_e64 s[6:7], 0, v15
	v_or_b32_e32 v252, v1, v3
	v_and_b32_e32 v2, 0xffffff80, v15
	v_xor_b32_e32 v0, 36, v66
	v_or_b32_e32 v188, 0x5b, v66
	v_cndmask_b32_e64 v0, v0, v188, s[6:7]
	v_cmp_gt_i32_e64 s[6:7], 0, v14
	v_and_b32_e32 v3, 0xffffff80, v14
	v_or_b32_e32 v190, v0, v2
	v_xor_b32_e32 v1, 37, v66
	v_or_b32_e32 v188, 0x5a, v66
	v_cndmask_b32_e64 v1, v1, v188, s[6:7]
	v_or_b32_e32 v195, v1, v3
	s_waitcnt vmcnt(7)
	v_mfma_f32_32x32x16_bf16 v[0:15], v[156:159], v[44:47], 0
	s_waitcnt vmcnt(6)
	v_mfma_f32_32x32x16_bf16 v[0:15], v[160:163], v[40:43], v[0:15]
	s_waitcnt vmcnt(5)
	v_mfma_f32_32x32x16_bf16 v[0:15], v[164:167], v[36:39], v[0:15]
	s_waitcnt vmcnt(4)
	v_mfma_f32_32x32x16_bf16 v[0:15], v[168:171], v[32:35], v[0:15]
	s_waitcnt vmcnt(3)
	v_mfma_f32_32x32x16_bf16 v[0:15], v[48:51], v[28:31], v[0:15]
	s_waitcnt vmcnt(2)
	v_mfma_f32_32x32x16_bf16 v[0:15], v[52:55], v[24:27], v[0:15]
	s_waitcnt vmcnt(1)
	v_mfma_f32_32x32x16_bf16 v[0:15], v[56:59], v[20:23], v[0:15]
	s_waitcnt vmcnt(0)
	v_mfma_f32_32x32x16_bf16 v[0:15], v[60:63], v[16:19], v[0:15]
	s_nop 11
	v_cmp_gt_i32_e64 s[6:7], 0, v1
	v_and_b32_e32 v1, 0xffffff80, v1
	v_and_b32_e32 v18, 0xffffff80, v0
	v_xor_b32_e32 v16, 30, v66
	v_or_b32_e32 v188, 0x61, v66
	v_cndmask_b32_e64 v16, v16, v188, s[6:7]
	v_cmp_gt_i32_e64 s[6:7], 0, v0
	v_or_b32_e32 v0, v16, v1
	v_xor_b32_e32 v17, 31, v66
	v_or_b32_e32 v188, 0x60, v66
	v_cndmask_b32_e64 v17, v17, v188, s[6:7]
	v_cmp_gt_i32_e64 s[6:7], 0, v3
	v_or_b32_e32 v1, v17, v18
	v_and_b32_e32 v3, 0xffffff80, v3
	v_xor_b32_e32 v16, 28, v66
	v_or_b32_e32 v188, 0x63, v66
	v_cndmask_b32_e64 v16, v16, v188, s[6:7]
	v_cmp_gt_i32_e64 s[6:7], 0, v2
	v_and_b32_e32 v18, 0xffffff80, v2
	v_or_b32_e32 v2, v16, v3
	v_xor_b32_e32 v17, 29, v66
	v_or_b32_e32 v188, 0x62, v66
	v_cndmask_b32_e64 v17, v17, v188, s[6:7]
	v_cmp_gt_i32_e64 s[6:7], 0, v5
	v_or_b32_e32 v3, v17, v18
	v_and_b32_e32 v5, 0xffffff80, v5
	v_xor_b32_e32 v16, 22, v66
	v_or_b32_e32 v188, 0x69, v66
	v_cndmask_b32_e64 v16, v16, v188, s[6:7]
	v_cmp_gt_i32_e64 s[6:7], 0, v4
	v_and_b32_e32 v18, 0xffffff80, v4
	v_or_b32_e32 v4, v16, v5
	v_xor_b32_e32 v17, 23, v66
	v_or_b32_e32 v188, 0x68, v66
	v_cndmask_b32_e64 v17, v17, v188, s[6:7]
	v_cmp_gt_i32_e64 s[6:7], 0, v7
	v_or_b32_e32 v5, v17, v18
	v_and_b32_e32 v7, 0xffffff80, v7
	v_xor_b32_e32 v16, 20, v66
	v_or_b32_e32 v188, 0x6b, v66
	v_cndmask_b32_e64 v16, v16, v188, s[6:7]
	v_cmp_gt_i32_e64 s[6:7], 0, v6
	v_and_b32_e32 v18, 0xffffff80, v6
	v_or_b32_e32 v6, v16, v7
	v_xor_b32_e32 v17, 21, v66
	v_or_b32_e32 v188, 0x6a, v66
	v_cndmask_b32_e64 v17, v17, v188, s[6:7]
	v_cmp_gt_i32_e64 s[6:7], 0, v9
	v_or_b32_e32 v7, v17, v18
	v_and_b32_e32 v9, 0xffffff80, v9
	v_xor_b32_e32 v16, 14, v66
	v_or_b32_e32 v188, 0x71, v66
	v_cndmask_b32_e64 v16, v16, v188, s[6:7]
	v_cmp_gt_i32_e64 s[6:7], 0, v8
	v_and_b32_e32 v18, 0xffffff80, v8
	v_or_b32_e32 v8, v16, v9
	v_xor_b32_e32 v17, 15, v66
	v_or_b32_e32 v188, 0x70, v66
	v_cndmask_b32_e64 v17, v17, v188, s[6:7]
	v_cmp_gt_i32_e64 s[6:7], 0, v11
	v_or_b32_e32 v9, v17, v18
	v_and_b32_e32 v11, 0xffffff80, v11
	v_xor_b32_e32 v16, 12, v66
	v_or_b32_e32 v188, 0x73, v66
	v_cndmask_b32_e64 v16, v16, v188, s[6:7]
	v_cmp_gt_i32_e64 s[6:7], 0, v10
	v_and_b32_e32 v18, 0xffffff80, v10
	v_or_b32_e32 v10, v16, v11
	v_xor_b32_e32 v17, 13, v66
	v_or_b32_e32 v188, 0x72, v66
	v_cndmask_b32_e64 v17, v17, v188, s[6:7]
	v_cmp_gt_i32_e64 s[6:7], 0, v13
	v_or_b32_e32 v11, v17, v18
	v_and_b32_e32 v13, 0xffffff80, v13
	v_xor_b32_e32 v16, 6, v66
	v_or_b32_e32 v188, 0x79, v66
	v_cndmask_b32_e64 v16, v16, v188, s[6:7]
	v_cmp_gt_i32_e64 s[6:7], 0, v12
	v_and_b32_e32 v18, 0xffffff80, v12
	v_or_b32_e32 v12, v16, v13
	v_xor_b32_e32 v17, 7, v66
	v_or_b32_e32 v188, 0x78, v66
	v_cndmask_b32_e64 v17, v17, v188, s[6:7]
	v_cmp_gt_i32_e64 s[6:7], 0, v15
	v_or_b32_e32 v16, v17, v18
	v_and_b32_e32 v15, 0xffffff80, v15
	v_xor_b32_e32 v13, 4, v66
	v_or_b32_e32 v188, 0x7b, v66
	v_cndmask_b32_e64 v13, v13, v188, s[6:7]
	v_cmp_gt_i32_e64 s[6:7], 0, v14
	v_and_b32_e32 v14, 0xffffff80, v14
	v_or_b32_e32 v25, v13, v15
	v_xor_b32_e32 v17, 5, v66
	v_or_b32_e32 v188, 0x7a, v66
	v_cndmask_b32_e64 v17, v17, v188, s[6:7]
	v_or_b32_e32 v28, v17, v14
	v_max_f32_e32 v13, v211, v221
	v_min_f32_e32 v221, v211, v221
	v_max_f32_e32 v14, v210, v222
	v_min_f32_e32 v222, v210, v222
	v_max_f32_e32 v15, v212, v223
	v_min_f32_e32 v223, v212, v223
	v_max_f32_e32 v17, v173, v224
	v_min_f32_e32 v224, v173, v224
	v_max_f32_e32 v18, v214, v218
	v_min_f32_e32 v218, v214, v218
	v_max_f32_e32 v19, v213, v216
	v_min_f32_e32 v216, v213, v216
	v_max_f32_e32 v20, v215, v219
	v_min_f32_e32 v219, v215, v219
	v_max_f32_e32 v21, v217, v220
	v_min_f32_e32 v220, v217, v220
	v_max_f32_e32 v22, v13, v19
	v_min_f32_e32 v19, v13, v19
	v_max_f32_e32 v23, v14, v20
	v_min_f32_e32 v20, v14, v20
	v_max_f32_e32 v24, v15, v21
	v_min_f32_e32 v21, v15, v21
	v_max_f32_e32 v26, v17, v18
	v_min_f32_e32 v18, v17, v18
	v_max_f32_e32 v27, v216, v221
	v_min_f32_e32 v221, v216, v221
	v_max_f32_e32 v29, v218, v224
	v_min_f32_e32 v224, v218, v224
	v_max_f32_e32 v30, v220, v223
	v_min_f32_e32 v223, v220, v223
	v_max_f32_e32 v31, v219, v222
	v_min_f32_e32 v222, v219, v222
	v_max_f32_e32 v32, v22, v23
	v_min_f32_e32 v23, v22, v23
	v_max_f32_e32 v33, v24, v26
	v_min_f32_e32 v26, v24, v26
	v_max_f32_e32 v34, v18, v19
	v_min_f32_e32 v19, v18, v19
	v_max_f32_e32 v35, v27, v29
	v_min_f32_e32 v29, v27, v29
	v_max_f32_e32 v36, v20, v21
	v_min_f32_e32 v21, v20, v21
	v_max_f32_e32 v37, v30, v31
	v_min_f32_e32 v31, v30, v31
	v_max_f32_e32 v38, v222, v221
	v_min_f32_e32 v221, v222, v221
	v_max_f32_e32 v39, v224, v223
	v_min_f32_e32 v223, v224, v223
	v_max_f32_e32 v40, v32, v33
	v_min_f32_e32 v33, v32, v33
	v_max_f32_e32 v41, v23, v26
	v_min_f32_e32 v26, v23, v26
	v_max_f32_e32 v42, v34, v37
	v_min_f32_e32 v37, v34, v37
	v_max_f32_e32 v43, v19, v31
	v_min_f32_e32 v31, v19, v31
	v_max_f32_e32 v44, v35, v36
	v_min_f32_e32 v36, v35, v36
	v_max_f32_e32 v45, v29, v21
	v_min_f32_e32 v21, v29, v21
	v_max_f32_e32 v46, v38, v39
	v_min_f32_e32 v39, v38, v39
	v_max_f32_e32 v47, v221, v223
	v_min_f32_e32 v223, v221, v223
	v_max_f32_e32 v48, v41, v33
	v_min_f32_e32 v33, v41, v33
	v_max_f32_e32 v49, v26, v46
	v_min_f32_e32 v46, v26, v46
	v_max_f32_e32 v50, v42, v44
	v_min_f32_e32 v44, v42, v44
	v_max_f32_e32 v51, v43, v36
	v_min_f32_e32 v36, v43, v36
	v_max_f32_e32 v52, v45, v37
	v_min_f32_e32 v37, v45, v37
	v_max_f32_e32 v53, v21, v31
	v_min_f32_e32 v31, v21, v31
	v_max_f32_e32 v54, v47, v39
	v_min_f32_e32 v39, v47, v39
	v_max_f32_e32 v55, v48, v50
	v_min_f32_e32 v50, v48, v50
	v_max_f32_e32 v56, v33, v44
	v_min_f32_e32 v44, v33, v44
	v_max_f32_e32 v57, v51, v52
	v_min_f32_e32 v52, v51, v52
	v_max_f32_e32 v58, v36, v37
	v_min_f32_e32 v37, v36, v37
	v_max_f32_e32 v59, v53, v54
	v_min_f32_e32 v54, v53, v54
	v_max_f32_e32 v60, v31, v39
	v_min_f32_e32 v39, v31, v39
	v_max_f32_e32 v61, v56, v50
	v_min_f32_e32 v50, v56, v50
	v_max_f32_e32 v62, v49, v44
	v_min_f32_e32 v44, v49, v44
	v_max_f32_e32 v63, v59, v46
	v_min_f32_e32 v46, v59, v46
	v_max_f32_e32 v211, v60, v54
	v_min_f32_e32 v54, v60, v54
	v_max_f32_e32 v210, v62, v57
	v_min_f32_e32 v57, v62, v57
	v_max_f32_e32 v212, v44, v52
	v_min_f32_e32 v52, v44, v52
	v_max_f32_e32 v173, v58, v63
	v_min_f32_e32 v63, v58, v63
	v_max_f32_e32 v214, v37, v46
	v_min_f32_e32 v46, v37, v46
	v_max_f32_e32 v213, v210, v50
	v_min_f32_e32 v50, v210, v50
	v_max_f32_e32 v215, v57, v212
	v_min_f32_e32 v212, v57, v212
	v_max_f32_e32 v217, v173, v52
	v_min_f32_e32 v52, v173, v52
	v_max_f32_e32 v13, v63, v214
	v_min_f32_e32 v214, v63, v214
	v_max_f32_e32 v14, v211, v46
	v_min_f32_e32 v46, v211, v46
	v_max_f32_e32 v15, v212, v217
	v_min_f32_e32 v217, v212, v217
	v_max_f32_e32 v17, v52, v13
	v_min_f32_e32 v13, v52, v13
	v_max_f32_e32 v216, v226, v237
	v_min_f32_e32 v237, v226, v237
	v_max_f32_e32 v218, v225, v238
	v_min_f32_e32 v238, v225, v238
	v_max_f32_e32 v220, v228, v239
	v_min_f32_e32 v239, v228, v239
	v_max_f32_e32 v219, v227, v240
	v_min_f32_e32 v240, v227, v240
	v_max_f32_e32 v22, v230, v234
	v_min_f32_e32 v234, v230, v234
	v_max_f32_e32 v24, v229, v232
	v_min_f32_e32 v232, v229, v232
	v_max_f32_e32 v18, v231, v235
	v_min_f32_e32 v235, v231, v235
	v_max_f32_e32 v27, v233, v236
	v_min_f32_e32 v236, v233, v236
	v_max_f32_e32 v20, v216, v24
	v_min_f32_e32 v24, v216, v24
	v_max_f32_e32 v30, v218, v18
	v_min_f32_e32 v18, v218, v18
	v_max_f32_e32 v222, v220, v27
	v_min_f32_e32 v27, v220, v27
	v_max_f32_e32 v224, v219, v22
	v_min_f32_e32 v22, v219, v22
	v_max_f32_e32 v32, v232, v237
	v_min_f32_e32 v237, v232, v237
	v_max_f32_e32 v23, v234, v240
	v_min_f32_e32 v240, v234, v240
	v_max_f32_e32 v34, v236, v239
	v_min_f32_e32 v239, v236, v239
	v_max_f32_e32 v19, v235, v238
	v_min_f32_e32 v238, v235, v238
	v_max_f32_e32 v35, v20, v30
	v_min_f32_e32 v30, v20, v30
	v_max_f32_e32 v29, v222, v224
	v_min_f32_e32 v224, v222, v224
	v_max_f32_e32 v38, v22, v24
	v_min_f32_e32 v24, v22, v24
	v_max_f32_e32 v221, v32, v23
	v_min_f32_e32 v23, v32, v23
	v_max_f32_e32 v41, v18, v27
	v_min_f32_e32 v27, v18, v27
	v_max_f32_e32 v26, v34, v19
	v_min_f32_e32 v19, v34, v19
	v_max_f32_e32 v42, v238, v237
	v_min_f32_e32 v237, v238, v237
	v_max_f32_e32 v43, v240, v239
	v_min_f32_e32 v239, v240, v239
	v_max_f32_e32 v45, v35, v29
	v_min_f32_e32 v29, v35, v29
	v_max_f32_e32 v21, v30, v224
	v_min_f32_e32 v224, v30, v224
	v_max_f32_e32 v47, v38, v26
	v_min_f32_e32 v26, v38, v26
	v_max_f32_e32 v48, v24, v19
	v_min_f32_e32 v19, v24, v19
	v_max_f32_e32 v33, v221, v41
	v_min_f32_e32 v41, v221, v41
	v_max_f32_e32 v51, v23, v27
	v_min_f32_e32 v27, v23, v27
	v_max_f32_e32 v36, v42, v43
	v_min_f32_e32 v43, v42, v43
	v_max_f32_e32 v53, v237, v239
	v_min_f32_e32 v239, v237, v239
	v_max_f32_e32 v31, v21, v29
	v_min_f32_e32 v29, v21, v29
	v_max_f32_e32 v56, v224, v36
	v_min_f32_e32 v36, v224, v36
	v_max_f32_e32 v49, v47, v33
	v_min_f32_e32 v33, v47, v33
	v_max_f32_e32 v59, v48, v41
	v_min_f32_e32 v41, v48, v41
	v_max_f32_e32 v60, v51, v26
	v_min_f32_e32 v26, v51, v26
	v_max_f32_e32 v62, v27, v19
	v_min_f32_e32 v19, v27, v19
	v_max_f32_e32 v44, v53, v43
	v_min_f32_e32 v43, v53, v43
	v_max_f32_e32 v58, v31, v49
	v_min_f32_e32 v49, v31, v49
	v_max_f32_e32 v37, v29, v33
	v_min_f32_e32 v33, v29, v33
	v_max_f32_e32 v210, v59, v60
	v_min_f32_e32 v60, v59, v60
	v_max_f32_e32 v57, v41, v26
	v_min_f32_e32 v26, v41, v26
	v_max_f32_e32 v173, v62, v44
	v_min_f32_e32 v44, v62, v44
	v_max_f32_e32 v63, v19, v43
	v_min_f32_e32 v43, v19, v43
	v_max_f32_e32 v211, v37, v49
	v_min_f32_e32 v49, v37, v49
	v_max_f32_e32 v212, v56, v33
	v_min_f32_e32 v33, v56, v33
	v_max_f32_e32 v52, v173, v36
	v_min_f32_e32 v36, v173, v36
	v_max_f32_e32 v226, v63, v44
	v_min_f32_e32 v44, v63, v44
	v_max_f32_e32 v225, v212, v210
	v_min_f32_e32 v210, v212, v210
	v_max_f32_e32 v228, v33, v60
	v_min_f32_e32 v60, v33, v60
	v_max_f32_e32 v227, v57, v52
	v_min_f32_e32 v52, v57, v52
	v_max_f32_e32 v230, v26, v36
	v_min_f32_e32 v36, v26, v36
	v_max_f32_e32 v229, v225, v49
	v_min_f32_e32 v49, v225, v49
	v_max_f32_e32 v231, v210, v228
	v_min_f32_e32 v228, v210, v228
	v_max_f32_e32 v233, v227, v60
	v_min_f32_e32 v60, v227, v60
	v_max_f32_e32 v216, v52, v230
	v_min_f32_e32 v230, v52, v230
	v_max_f32_e32 v218, v226, v36
	v_min_f32_e32 v36, v226, v36
	v_max_f32_e32 v220, v228, v233
	v_min_f32_e32 v233, v228, v233
	v_max_f32_e32 v219, v60, v216
	v_min_f32_e32 v216, v60, v216
	v_max_f32_e32 v232, v183, v251
	v_min_f32_e32 v251, v183, v251
	v_max_f32_e32 v234, v182, v252
	v_min_f32_e32 v252, v182, v252
	v_max_f32_e32 v236, v242, v190
	v_min_f32_e32 v190, v242, v190
	v_max_f32_e32 v235, v241, v195
	v_min_f32_e32 v195, v241, v195
	v_max_f32_e32 v20, v244, v248
	v_min_f32_e32 v248, v244, v248
	v_max_f32_e32 v222, v243, v246
	v_min_f32_e32 v246, v243, v246
	v_max_f32_e32 v22, v245, v249
	v_min_f32_e32 v249, v245, v249
	v_max_f32_e32 v32, v247, v250
	v_min_f32_e32 v250, v247, v250
	v_max_f32_e32 v18, v232, v222
	v_min_f32_e32 v222, v232, v222
	v_max_f32_e32 v34, v234, v22
	v_min_f32_e32 v22, v234, v22
	v_max_f32_e32 v238, v236, v32
	v_min_f32_e32 v32, v236, v32
	v_max_f32_e32 v240, v235, v20
	v_min_f32_e32 v20, v235, v20
	v_max_f32_e32 v35, v246, v251
	v_min_f32_e32 v251, v246, v251
	v_max_f32_e32 v30, v248, v195
	v_min_f32_e32 v195, v248, v195
	v_max_f32_e32 v38, v250, v190
	v_min_f32_e32 v190, v250, v190
	v_max_f32_e32 v24, v249, v252
	v_min_f32_e32 v252, v249, v252
	v_max_f32_e32 v221, v18, v34
	v_min_f32_e32 v34, v18, v34
	v_max_f32_e32 v23, v238, v240
	v_min_f32_e32 v240, v238, v240
	v_max_f32_e32 v42, v20, v222
	v_min_f32_e32 v222, v20, v222
	v_max_f32_e32 v237, v35, v30
	v_min_f32_e32 v30, v35, v30
	v_max_f32_e32 v21, v22, v32
	v_min_f32_e32 v32, v22, v32
	v_max_f32_e32 v224, v38, v24
	v_min_f32_e32 v24, v38, v24
	v_max_f32_e32 v47, v252, v251
	v_min_f32_e32 v251, v252, v251
	v_max_f32_e32 v48, v195, v190
	v_min_f32_e32 v190, v195, v190
	v_max_f32_e32 v51, v221, v23
	v_min_f32_e32 v23, v221, v23
	v_max_f32_e32 v27, v34, v240
	v_min_f32_e32 v240, v34, v240
	v_max_f32_e32 v53, v42, v224
	v_min_f32_e32 v224, v42, v224
	v_max_f32_e32 v31, v222, v24
	v_min_f32_e32 v24, v222, v24
	v_max_f32_e32 v29, v237, v21
	v_min_f32_e32 v21, v237, v21
	v_max_f32_e32 v59, v30, v32
	v_min_f32_e32 v32, v30, v32
	v_max_f32_e32 v41, v47, v48
	v_min_f32_e32 v48, v47, v48
	v_max_f32_e32 v62, v251, v190
	v_min_f32_e32 v190, v251, v190
	v_max_f32_e32 v19, v27, v23
	v_min_f32_e32 v23, v27, v23
	v_max_f32_e32 v37, v240, v41
	v_min_f32_e32 v41, v240, v41
	v_max_f32_e32 v56, v53, v29
	v_min_f32_e32 v29, v53, v29
	v_max_f32_e32 v173, v31, v21
	v_min_f32_e32 v21, v31, v21
	v_max_f32_e32 v63, v59, v224
	v_min_f32_e32 v224, v59, v224
	v_max_f32_e32 v212, v32, v24
	v_min_f32_e32 v24, v32, v24
	v_max_f32_e32 v33, v62, v48
	v_min_f32_e32 v48, v62, v48
	v_max_f32_e32 v57, v19, v56
	v_min_f32_e32 v56, v19, v56
	v_max_f32_e32 v26, v23, v29
	v_min_f32_e32 v29, v23, v29
	v_max_f32_e32 v225, v173, v63
	v_min_f32_e32 v63, v173, v63
	v_max_f32_e32 v210, v21, v224
	v_min_f32_e32 v224, v21, v224
	v_max_f32_e32 v227, v212, v33
	v_min_f32_e32 v33, v212, v33
	v_max_f32_e32 v52, v24, v48
	v_min_f32_e32 v48, v24, v48
	v_max_f32_e32 v226, v26, v56
	v_min_f32_e32 v56, v26, v56
	v_max_f32_e32 v228, v37, v29
	v_min_f32_e32 v29, v37, v29
	v_max_f32_e32 v60, v227, v41
	v_min_f32_e32 v41, v227, v41
	v_max_f32_e32 v183, v52, v33
	v_min_f32_e32 v33, v52, v33
	v_max_f32_e32 v182, v228, v225
	v_min_f32_e32 v225, v228, v225
	v_max_f32_e32 v242, v29, v63
	v_min_f32_e32 v63, v29, v63
	v_max_f32_e32 v241, v210, v60
	v_min_f32_e32 v60, v210, v60
	v_max_f32_e32 v244, v224, v41
	v_min_f32_e32 v41, v224, v41
	v_max_f32_e32 v243, v182, v56
	v_min_f32_e32 v56, v182, v56
	v_max_f32_e32 v245, v225, v242
	v_min_f32_e32 v242, v225, v242
	v_max_f32_e32 v247, v241, v63
	v_min_f32_e32 v63, v241, v63
	v_max_f32_e32 v232, v60, v244
	v_min_f32_e32 v244, v60, v244
	v_max_f32_e32 v234, v183, v41
	v_min_f32_e32 v41, v183, v41
	v_max_f32_e32 v236, v242, v247
	v_min_f32_e32 v247, v242, v247
	v_max_f32_e32 v235, v63, v232
	v_min_f32_e32 v232, v63, v232
	v_max_f32_e32 v246, v1, v12
	v_min_f32_e32 v12, v1, v12
	v_max_f32_e32 v248, v0, v16
	v_min_f32_e32 v16, v0, v16
	v_max_f32_e32 v250, v3, v25
	v_min_f32_e32 v25, v3, v25
	v_max_f32_e32 v249, v2, v28
	v_min_f32_e32 v28, v2, v28
	v_max_f32_e32 v18, v5, v9
	v_min_f32_e32 v9, v5, v9
	v_max_f32_e32 v238, v4, v7
	v_min_f32_e32 v7, v4, v7
	v_max_f32_e32 v20, v6, v10
	v_min_f32_e32 v10, v6, v10
	v_max_f32_e32 v35, v8, v11
	v_min_f32_e32 v11, v8, v11
	v_max_f32_e32 v22, v246, v238
	v_min_f32_e32 v238, v246, v238
	v_max_f32_e32 v38, v248, v20
	v_min_f32_e32 v20, v248, v20
	v_max_f32_e32 v252, v250, v35
	v_min_f32_e32 v35, v250, v35
	v_max_f32_e32 v195, v249, v18
	v_min_f32_e32 v18, v249, v18
	v_max_f32_e32 v221, v7, v12
	v_min_f32_e32 v12, v7, v12
	v_max_f32_e32 v34, v9, v28
	v_min_f32_e32 v28, v9, v28
	v_max_f32_e32 v42, v11, v25
	v_min_f32_e32 v25, v11, v25
	v_max_f32_e32 v222, v10, v16
	v_min_f32_e32 v16, v10, v16
	v_max_f32_e32 v237, v22, v38
	v_min_f32_e32 v38, v22, v38
	v_max_f32_e32 v30, v252, v195
	v_min_f32_e32 v195, v252, v195
	v_max_f32_e32 v47, v18, v238
	v_min_f32_e32 v238, v18, v238
	v_max_f32_e32 v251, v221, v34
	v_min_f32_e32 v34, v221, v34
	v_max_f32_e32 v27, v20, v35
	v_min_f32_e32 v35, v20, v35
	v_max_f32_e32 v240, v42, v222
	v_min_f32_e32 v222, v42, v222
	v_max_f32_e32 v53, v16, v12
	v_min_f32_e32 v12, v16, v12
	v_max_f32_e32 v31, v28, v25
	v_min_f32_e32 v25, v28, v25
	v_max_f32_e32 v59, v237, v30
	v_min_f32_e32 v30, v237, v30
	v_max_f32_e32 v32, v38, v195
	v_min_f32_e32 v195, v38, v195
	v_max_f32_e32 v62, v47, v240
	v_min_f32_e32 v240, v47, v240
	v_max_f32_e32 v19, v238, v222
	v_min_f32_e32 v222, v238, v222
	v_max_f32_e32 v23, v251, v27
	v_min_f32_e32 v27, v251, v27
	v_max_f32_e32 v173, v34, v35
	v_min_f32_e32 v35, v34, v35
	v_max_f32_e32 v21, v53, v31
	v_min_f32_e32 v31, v53, v31
	v_max_f32_e32 v212, v12, v25
	v_min_f32_e32 v25, v12, v25
	v_max_f32_e32 v24, v32, v30
	v_min_f32_e32 v30, v32, v30
	v_max_f32_e32 v26, v195, v21
	v_min_f32_e32 v21, v195, v21
	v_max_f32_e32 v37, v62, v23
	v_min_f32_e32 v23, v62, v23
	v_max_f32_e32 v227, v19, v27
	v_min_f32_e32 v27, v19, v27
	v_max_f32_e32 v52, v173, v240
	v_min_f32_e32 v240, v173, v240
	v_max_f32_e32 v228, v35, v222
	v_min_f32_e32 v222, v35, v222
	v_max_f32_e32 v29, v212, v31
	v_min_f32_e32 v31, v212, v31
	v_max_f32_e32 v210, v24, v37
	v_min_f32_e32 v37, v24, v37
	v_max_f32_e32 v224, v30, v23
	v_min_f32_e32 v23, v30, v23
	v_max_f32_e32 v182, v227, v52
	v_min_f32_e32 v52, v227, v52
	v_max_f32_e32 v225, v27, v240
	v_min_f32_e32 v240, v27, v240
	v_max_f32_e32 v241, v228, v29
	v_min_f32_e32 v29, v228, v29
	v_max_f32_e32 v60, v222, v31
	v_min_f32_e32 v31, v222, v31
	v_max_f32_e32 v183, v224, v37
	v_min_f32_e32 v37, v224, v37
	v_max_f32_e32 v242, v26, v23
	v_min_f32_e32 v23, v26, v23
	v_max_f32_e32 v63, v241, v21
	v_min_f32_e32 v21, v241, v21
	v_max_f32_e32 v1, v60, v29
	v_min_f32_e32 v29, v60, v29
	v_max_f32_e32 v0, v242, v182
	v_min_f32_e32 v182, v242, v182
	v_max_f32_e32 v3, v23, v52
	v_min_f32_e32 v52, v23, v52
	v_max_f32_e32 v2, v225, v63
	v_min_f32_e32 v63, v225, v63
	v_max_f32_e32 v5, v240, v21
	v_min_f32_e32 v21, v240, v21
	v_max_f32_e32 v4, v0, v37
	v_min_f32_e32 v37, v0, v37
	v_max_f32_e32 v6, v182, v3
	v_min_f32_e32 v3, v182, v3
	v_max_f32_e32 v8, v2, v52
	v_min_f32_e32 v52, v2, v52
	v_max_f32_e32 v246, v63, v5
	v_min_f32_e32 v5, v63, v5
	v_max_f32_e32 v248, v1, v21
	v_min_f32_e32 v21, v1, v21
	v_max_f32_e32 v250, v3, v8
	v_min_f32_e32 v8, v3, v8
	v_max_f32_e32 v249, v52, v246
	v_min_f32_e32 v246, v52, v246
	v_max_f32_e32 v40, v40, v239
	v_max_f32_e32 v55, v55, v43
	v_max_f32_e32 v61, v61, v44
	v_max_f32_e32 v213, v213, v36
	v_max_f32_e32 v50, v50, v218
	v_max_f32_e32 v215, v215, v230
	v_max_f32_e32 v15, v15, v216
	v_max_f32_e32 v217, v217, v219
	v_max_f32_e32 v17, v17, v233
	v_max_f32_e32 v13, v13, v220
	v_max_f32_e32 v214, v214, v231
	v_max_f32_e32 v14, v14, v49
	v_max_f32_e32 v46, v46, v229
	v_max_f32_e32 v54, v54, v211
	v_max_f32_e32 v39, v39, v58
	v_max_f32_e32 v223, v223, v45
	v_max_f32_e32 v7, v40, v17
	v_min_f32_e32 v17, v40, v17
	v_max_f32_e32 v9, v55, v13
	v_min_f32_e32 v13, v55, v13
	v_max_f32_e32 v11, v61, v214
	v_min_f32_e32 v214, v61, v214
	v_max_f32_e32 v10, v213, v14
	v_min_f32_e32 v14, v213, v14
	v_max_f32_e32 v22, v50, v46
	v_min_f32_e32 v46, v50, v46
	v_max_f32_e32 v252, v215, v54
	v_min_f32_e32 v54, v215, v54
	v_max_f32_e32 v18, v15, v39
	v_min_f32_e32 v39, v15, v39
	v_max_f32_e32 v221, v217, v223
	v_min_f32_e32 v223, v217, v223
	v_max_f32_e32 v20, v7, v22
	v_min_f32_e32 v22, v7, v22
	v_max_f32_e32 v42, v9, v252
	v_min_f32_e32 v252, v9, v252
	v_max_f32_e32 v16, v11, v18
	v_min_f32_e32 v18, v11, v18
	v_max_f32_e32 v28, v10, v221
	v_min_f32_e32 v221, v10, v221
	v_max_f32_e32 v237, v17, v46
	v_min_f32_e32 v46, v17, v46
	v_max_f32_e32 v38, v13, v54
	v_min_f32_e32 v54, v13, v54
	v_max_f32_e32 v47, v214, v39
	v_min_f32_e32 v39, v214, v39
	v_max_f32_e32 v238, v14, v223
	v_min_f32_e32 v223, v14, v223
	v_max_f32_e32 v251, v20, v16
	v_min_f32_e32 v16, v20, v16
	v_max_f32_e32 v34, v42, v28
	v_min_f32_e32 v28, v42, v28
	v_max_f32_e32 v53, v22, v18
	v_min_f32_e32 v18, v22, v18
	v_max_f32_e32 v12, v252, v221
	v_min_f32_e32 v221, v252, v221
	v_max_f32_e32 v32, v237, v47
	v_min_f32_e32 v47, v237, v47
	v_max_f32_e32 v195, v38, v238
	v_min_f32_e32 v238, v38, v238
	v_max_f32_e32 v62, v46, v39
	v_min_f32_e32 v39, v46, v39
	v_max_f32_e32 v19, v54, v223
	v_min_f32_e32 v223, v54, v223
	v_max_f32_e32 v173, v251, v34
	v_min_f32_e32 v34, v251, v34
	v_max_f32_e32 v35, v16, v28
	v_min_f32_e32 v28, v16, v28
	v_max_f32_e32 v212, v53, v12
	v_min_f32_e32 v12, v53, v12
	v_max_f32_e32 v24, v18, v221
	v_min_f32_e32 v221, v18, v221
	v_max_f32_e32 v30, v32, v195
	v_min_f32_e32 v195, v32, v195
	v_max_f32_e32 v227, v47, v238
	v_min_f32_e32 v238, v47, v238
	v_max_f32_e32 v27, v62, v19
	v_min_f32_e32 v19, v62, v19
	v_max_f32_e32 v228, v39, v223
	v_min_f32_e32 v223, v39, v223
	v_max_f32_e32 v51, v51, v25
	v_max_f32_e32 v57, v57, v31
	v_max_f32_e32 v226, v226, v29
	v_max_f32_e32 v243, v243, v21
	v_max_f32_e32 v56, v56, v248
	v_max_f32_e32 v245, v245, v5
	v_max_f32_e32 v236, v236, v246
	v_max_f32_e32 v247, v247, v249
	v_max_f32_e32 v235, v235, v8
	v_max_f32_e32 v232, v232, v250
	v_max_f32_e32 v244, v244, v6
	v_max_f32_e32 v234, v234, v37
	v_max_f32_e32 v41, v41, v4
	v_max_f32_e32 v33, v33, v183
	v_max_f32_e32 v48, v48, v210
	v_max_f32_e32 v190, v190, v59
	v_max_f32_e32 v222, v51, v235
	v_min_f32_e32 v235, v51, v235
	v_max_f32_e32 v224, v57, v232
	v_min_f32_e32 v232, v57, v232
	v_max_f32_e32 v26, v226, v244
	v_min_f32_e32 v244, v226, v244
	v_max_f32_e32 v241, v243, v234
	v_min_f32_e32 v234, v243, v234
	v_max_f32_e32 v60, v56, v41
	v_min_f32_e32 v41, v56, v41
	v_max_f32_e32 v242, v245, v33
	v_min_f32_e32 v33, v245, v33
	v_max_f32_e32 v23, v236, v48
	v_min_f32_e32 v48, v236, v48
	v_max_f32_e32 v225, v247, v190
	v_min_f32_e32 v190, v247, v190
	v_max_f32_e32 v240, v222, v60
	v_min_f32_e32 v60, v222, v60
	v_max_f32_e32 v0, v224, v242
	v_min_f32_e32 v242, v224, v242
	v_max_f32_e32 v182, v26, v23
	v_min_f32_e32 v23, v26, v23
	v_max_f32_e32 v2, v241, v225
	v_min_f32_e32 v225, v241, v225
	v_max_f32_e32 v63, v235, v41
	v_min_f32_e32 v41, v235, v41
	v_max_f32_e32 v1, v232, v33
	v_min_f32_e32 v33, v232, v33
	v_max_f32_e32 v3, v244, v48
	v_min_f32_e32 v48, v244, v48
	v_max_f32_e32 v52, v234, v190
	v_min_f32_e32 v190, v234, v190
	v_max_f32_e32 v239, v240, v182
	v_min_f32_e32 v182, v240, v182
	v_max_f32_e32 v43, v0, v2
	v_min_f32_e32 v2, v0, v2
	v_max_f32_e32 v44, v60, v23
	v_min_f32_e32 v23, v60, v23
	v_max_f32_e32 v36, v242, v225
	v_min_f32_e32 v225, v242, v225
	v_max_f32_e32 v218, v63, v3
	v_min_f32_e32 v3, v63, v3
	v_max_f32_e32 v230, v1, v52
	v_min_f32_e32 v52, v1, v52
	v_max_f32_e32 v216, v41, v48
	v_min_f32_e32 v48, v41, v48
	v_max_f32_e32 v219, v33, v190
	v_min_f32_e32 v190, v33, v190
	v_max_f32_e32 v233, v239, v43
	v_min_f32_e32 v43, v239, v43
	v_max_f32_e32 v220, v182, v2
	v_min_f32_e32 v2, v182, v2
	v_max_f32_e32 v231, v44, v36
	v_min_f32_e32 v36, v44, v36
	v_max_f32_e32 v49, v23, v225
	v_min_f32_e32 v225, v23, v225
	v_max_f32_e32 v229, v218, v230
	v_min_f32_e32 v230, v218, v230
	v_max_f32_e32 v211, v3, v52
	v_min_f32_e32 v52, v3, v52
	v_max_f32_e32 v58, v216, v219
	v_min_f32_e32 v219, v216, v219
	v_max_f32_e32 v45, v48, v190
	v_min_f32_e32 v190, v48, v190
	v_max_f32_e32 v173, v173, v190
	v_max_f32_e32 v34, v34, v45
	v_max_f32_e32 v35, v35, v219
	v_max_f32_e32 v28, v28, v58
	v_max_f32_e32 v212, v212, v52
	v_max_f32_e32 v12, v12, v211
	v_max_f32_e32 v24, v24, v230
	v_max_f32_e32 v221, v221, v229
	v_max_f32_e32 v30, v30, v225
	v_max_f32_e32 v195, v195, v49
	v_max_f32_e32 v227, v227, v36
	v_max_f32_e32 v238, v238, v231
	v_max_f32_e32 v27, v27, v2
	v_max_f32_e32 v19, v19, v220
	v_max_f32_e32 v228, v228, v43
	v_max_f32_e32 v223, v223, v233
	v_max_f32_e32 v40, v173, v30
	v_min_f32_e32 v30, v173, v30
	v_max_f32_e32 v55, v34, v195
	v_min_f32_e32 v195, v34, v195
	v_max_f32_e32 v61, v35, v227
	v_min_f32_e32 v227, v35, v227
	v_max_f32_e32 v213, v28, v238
	v_min_f32_e32 v238, v28, v238
	v_max_f32_e32 v50, v212, v27
	v_min_f32_e32 v27, v212, v27
	v_max_f32_e32 v215, v12, v19
	v_min_f32_e32 v19, v12, v19
	v_max_f32_e32 v15, v24, v228
	v_min_f32_e32 v228, v24, v228
	v_max_f32_e32 v217, v221, v223
	v_min_f32_e32 v223, v221, v223
	v_max_f32_e32 v7, v40, v50
	v_min_f32_e32 v50, v40, v50
	v_max_f32_e32 v9, v55, v215
	v_min_f32_e32 v215, v55, v215
	v_max_f32_e32 v11, v61, v15
	v_min_f32_e32 v15, v61, v15
	v_max_f32_e32 v10, v213, v217
	v_min_f32_e32 v217, v213, v217
	v_max_f32_e32 v17, v30, v27
	v_min_f32_e32 v27, v30, v27
	v_max_f32_e32 v13, v195, v19
	v_min_f32_e32 v19, v195, v19
	v_max_f32_e32 v214, v227, v228
	v_min_f32_e32 v228, v227, v228
	v_max_f32_e32 v14, v238, v223
	v_min_f32_e32 v223, v238, v223
	v_max_f32_e32 v20, v7, v11
	v_min_f32_e32 v11, v7, v11
	v_max_f32_e32 v42, v9, v10
	v_min_f32_e32 v10, v9, v10
	v_max_f32_e32 v22, v50, v15
	v_min_f32_e32 v15, v50, v15
	v_max_f32_e32 v252, v215, v217
	v_min_f32_e32 v217, v215, v217
	v_max_f32_e32 v237, v17, v214
	v_min_f32_e32 v214, v17, v214
	v_max_f32_e32 v38, v13, v14
	v_min_f32_e32 v14, v13, v14
	v_max_f32_e32 v46, v27, v228
	v_min_f32_e32 v228, v27, v228
	v_max_f32_e32 v54, v19, v223
	v_min_f32_e32 v223, v19, v223
	v_max_f32_e32 v251, v20, v42
	v_min_f32_e32 v42, v20, v42
	v_max_f32_e32 v16, v11, v10
	v_min_f32_e32 v10, v11, v10
	v_max_f32_e32 v53, v22, v252
	v_min_f32_e32 v252, v22, v252
	v_max_f32_e32 v18, v15, v217
	v_min_f32_e32 v217, v15, v217
	v_max_f32_e32 v32, v237, v38
	v_min_f32_e32 v38, v237, v38
	v_max_f32_e32 v47, v214, v14
	v_min_f32_e32 v14, v214, v14
	v_max_f32_e32 v62, v46, v54
	v_min_f32_e32 v54, v46, v54
	v_max_f32_e32 v39, v228, v223
	v_min_f32_e32 v223, v228, v223
	v_mov_b32_e32 v2, v251
	v_mov_b32_e32 v9, v42
	v_mov_b32_e32 v11, v16
	v_mov_b32_e32 v6, v10
	v_mov_b32_e32 v15, v53
	v_mov_b32_e32 v16, v18
	v_mov_b32_e32 v5, v217
	v_mov_b32_e32 v12, v32
	v_mov_b32_e32 v10, v38
	v_mov_b32_e32 v13, v47
	v_mov_b32_e32 v4, v14
	v_mov_b32_e32 v8, v62
	v_mov_b32_e32 v3, v54
	v_mov_b32_e32 v7, v39
	v_mov_b32_e32 v0, v223
	v_mov_b32_e32 v14, v252
	v_mov_b32_e32 v27, v0
	s_nop 1
	v_permlane32_swap_b32 v27, v27
	v_mov_b32_e32 v29, v7
	s_nop 1
	v_permlane32_swap_b32 v29, v29
	v_mov_b32_e32 v31, v3
	s_nop 1
	v_permlane32_swap_b32 v31, v31
	v_mov_b32_e32 v30, v8
	s_nop 1
	v_permlane32_swap_b32 v30, v30
	v_mov_b32_e32 v28, v4
	s_nop 1
	v_permlane32_swap_b32 v28, v28
	v_mov_b32_e32 v26, v13
	s_nop 1
	v_permlane32_swap_b32 v26, v26
	s_waitcnt lgkmcnt(5)
	v_mov_b32_e32 v1, v2
	s_nop 1
	v_permlane32_swap_b32 v1, v1
	v_mov_b32_e32 v25, v10
	s_nop 1
	v_permlane32_swap_b32 v25, v25
	v_max_f32_e32 v2, v2, v27
	s_waitcnt lgkmcnt(6)
	v_mov_b32_e32 v17, v9
	s_nop 1
	v_permlane32_swap_b32 v17, v17
	v_mov_b32_e32 v24, v12
	s_nop 1
	v_permlane32_swap_b32 v24, v24
	v_max_f32_e32 v9, v9, v29
	s_waitcnt lgkmcnt(7)
	v_mov_b32_e32 v18, v11
	s_nop 1
	v_permlane32_swap_b32 v18, v18
	v_mov_b32_e32 v23, v5
	s_nop 1
	v_permlane32_swap_b32 v23, v23
	v_max_f32_e32 v11, v11, v31
	s_waitcnt lgkmcnt(8)
	v_mov_b32_e32 v19, v6
	s_nop 1
	v_permlane32_swap_b32 v19, v19
	v_mov_b32_e32 v22, v16
	s_nop 1
	v_permlane32_swap_b32 v22, v22
	v_max_f32_e32 v6, v6, v30
	s_waitcnt lgkmcnt(9)
	v_mov_b32_e32 v20, v15
	s_nop 1
	v_permlane32_swap_b32 v20, v20
	v_mov_b32_e32 v21, v14
	s_nop 1
	v_permlane32_swap_b32 v21, v21
	v_max_f32_e32 v15, v15, v28
	s_waitcnt lgkmcnt(10)
	v_max_f32_e32 v14, v14, v26
	s_waitcnt lgkmcnt(8)
	v_max_f32_e32 v16, v16, v25
	s_waitcnt lgkmcnt(6)
	v_max_f32_e32 v5, v5, v24
	s_waitcnt lgkmcnt(4)
	v_max_f32_e32 v12, v12, v23
	s_waitcnt lgkmcnt(2)
	v_max_f32_e32 v10, v10, v22
	s_waitcnt lgkmcnt(0)
	v_max_f32_e32 v13, v13, v21
	v_max_f32_e32 v4, v4, v20
	v_max_f32_e32 v8, v8, v19
	v_max_f32_e32 v3, v3, v18
	v_max_f32_e32 v7, v7, v17
	v_max_f32_e32 v0, v0, v1
	v_max_f32_e32 v1, v2, v12
	v_min_f32_e32 v2, v2, v12
	v_max_f32_e32 v12, v9, v10
	v_min_f32_e32 v9, v9, v10
	v_max_f32_e32 v10, v11, v13
	v_min_f32_e32 v11, v11, v13
	v_max_f32_e32 v13, v6, v4
	v_min_f32_e32 v4, v6, v4
	v_max_f32_e32 v6, v15, v8
	v_min_f32_e32 v8, v15, v8
	v_max_f32_e32 v15, v14, v3
	v_min_f32_e32 v3, v14, v3
	v_max_f32_e32 v14, v16, v7
	v_min_f32_e32 v7, v16, v7
	v_max_f32_e32 v16, v5, v0
	v_min_f32_e32 v0, v5, v0
	v_max_f32_e32 v5, v1, v6
	v_min_f32_e32 v1, v1, v6
	v_max_f32_e32 v6, v12, v15
	v_min_f32_e32 v12, v12, v15
	v_max_f32_e32 v15, v10, v14
	v_min_f32_e32 v10, v10, v14
	v_max_f32_e32 v14, v13, v16
	v_min_f32_e32 v13, v13, v16
	v_max_f32_e32 v16, v2, v8
	v_min_f32_e32 v2, v2, v8
	v_max_f32_e32 v8, v9, v3
	v_min_f32_e32 v3, v9, v3
	v_max_f32_e32 v9, v11, v7
	v_min_f32_e32 v7, v11, v7
	v_max_f32_e32 v11, v4, v0
	v_min_f32_e32 v0, v4, v0
	v_max_f32_e32 v4, v5, v15
	v_min_f32_e32 v5, v5, v15
	v_max_f32_e32 v15, v6, v14
	v_min_f32_e32 v6, v6, v14
	v_max_f32_e32 v14, v1, v10
	v_min_f32_e32 v1, v1, v10
	v_max_f32_e32 v10, v12, v13
	v_min_f32_e32 v12, v12, v13
	v_max_f32_e32 v13, v16, v9
	v_min_f32_e32 v9, v16, v9
	v_max_f32_e32 v16, v8, v11
	v_min_f32_e32 v8, v8, v11
	v_max_f32_e32 v11, v2, v7
	v_min_f32_e32 v2, v2, v7
	v_max_f32_e32 v7, v3, v0
	v_min_f32_e32 v0, v3, v0
	v_max_f32_e32 v3, v4, v15
	v_min_f32_e32 v4, v4, v15
	v_max_f32_e32 v15, v5, v6
	v_min_f32_e32 v5, v5, v6
	v_max_f32_e32 v6, v14, v10
	v_min_f32_e32 v10, v14, v10
	v_max_f32_e32 v14, v1, v12
	v_min_f32_e32 v1, v1, v12
	v_max_f32_e32 v12, v13, v16
	v_min_f32_e32 v13, v13, v16
	v_max_f32_e32 v16, v9, v8
	v_min_f32_e32 v8, v9, v8
	v_max_f32_e32 v9, v11, v7
	v_min_f32_e32 v7, v11, v7
	v_max_f32_e32 v11, v2, v0
	v_min_f32_e32 v0, v2, v0
	v_lshl_add_u32 v2, s8, 12, v207
	ds_write2st64_b32 v2, v3, v4 offset1:1
	ds_write2st64_b32 v2, v15, v5 offset0:2 offset1:3
	ds_write2st64_b32 v2, v6, v10 offset0:4 offset1:5
	ds_write2st64_b32 v2, v14, v1 offset0:6 offset1:7
	ds_write2st64_b32 v2, v12, v13 offset0:8 offset1:9
	ds_write2st64_b32 v2, v16, v8 offset0:10 offset1:11
	ds_write2st64_b32 v2, v9, v7 offset0:12 offset1:13
	ds_write2st64_b32 v2, v11, v0 offset0:14 offset1:15
	s_mov_b64 s[6:7], 0
	s_mov_b32 s8, 1
	s_cbranch_vccz .LBB0_704
	ds_read2st64_b32 v[0:1], v207 offset1:1
	ds_read2st64_b32 v[2:3], v207 offset0:2 offset1:3
	ds_read2st64_b32 v[4:5], v207 offset0:4 offset1:5
	ds_read2st64_b32 v[6:7], v207 offset0:6 offset1:7
	ds_read2st64_b32 v[16:17], v207 offset0:16 offset1:17
	ds_read2st64_b32 v[18:19], v207 offset0:18 offset1:19
	ds_read2st64_b32 v[20:21], v207 offset0:20 offset1:21
	ds_read2st64_b32 v[22:23], v207 offset0:22 offset1:23
	ds_read2st64_b32 v[8:9], v207 offset0:8 offset1:9
	ds_read2st64_b32 v[10:11], v207 offset0:10 offset1:11
	ds_read2st64_b32 v[12:13], v207 offset0:12 offset1:13
	ds_read2st64_b32 v[14:15], v207 offset0:14 offset1:15
	ds_read2st64_b32 v[24:25], v207 offset0:24 offset1:25
	ds_read2st64_b32 v[26:27], v207 offset0:26 offset1:27
	ds_read2st64_b32 v[28:29], v207 offset0:28 offset1:29
	ds_read2st64_b32 v[30:31], v207 offset0:30 offset1:31
	s_and_saveexec_b64 s[8:9], s[38:39]
	s_cbranch_execz .LBB0_696
	s_waitcnt lgkmcnt(0)
	v_and_b32_e32 v49, 0xffffff80, v30
	v_and_b32_e32 v48, 0xffffff80, v0
	v_and_b32_e32 v39, 0xffffff80, v19
	v_and_b32_e32 v38, 0xffffff80, v20
	v_pk_add_f32 v[52:53], v[38:39], v[48:49] op_sel:[1,0] op_sel_hi:[0,1]
	v_cmp_gt_i32_e32 vcc, 0, v52
	v_bfrev_b32_e32 v43, 0.5
	s_movk_i32 s12, 0xff00
	v_cndmask_b32_e64 v43, v43, 3, vcc
	v_and_b32_e32 v42, 0xffffff80, v23
	v_and_or_b32 v56, v52, s12, v43
	v_mov_b32_e32 v43, v38
	v_pk_add_f32 v[52:53], v[48:49], v[42:43] op_sel_hi:[0,1]
	v_cmp_gt_i32_e32 vcc, 0, v53
	v_mov_b32_e32 v54, 0xfb
	v_and_b32_e32 v41, 0xffffff80, v22
	v_cndmask_b32_e64 v54, v54, 4, vcc
	v_and_b32_e32 v40, 0xffffff80, v21
	v_and_or_b32 v53, v53, s12, v54
	v_cmp_gt_i32_e32 vcc, 0, v52
	v_mov_b32_e32 v54, 0xf8
	v_mov_b32_e32 v58, 0xf9
	v_cndmask_b32_e64 v57, v54, 7, vcc
	v_pk_add_f32 v[54:55], v[48:49], v[40:41] op_sel_hi:[0,1]
	v_cmp_gt_i32_e32 vcc, 0, v55
	v_mov_b32_e32 v59, 0xfa
	v_and_b32_e32 v55, 0xffffff00, v55
	v_cndmask_b32_e64 v58, v58, 6, vcc
	v_cmp_gt_i32_e32 vcc, 0, v54
	v_and_b32_e32 v54, 0xffffff00, v54
	v_and_b32_e32 v52, 0xffffff00, v52
	v_cndmask_b32_e64 v59, v59, 5, vcc
	v_or_b32_e32 v55, v58, v55
	v_or_b32_e32 v54, v59, v54
	v_or_b32_e32 v52, v57, v52
	v_writelane_b32 v255, s8, 44
	v_min_f32_e32 v57, v55, v52
	v_max_f32_e32 v58, v53, v54
	v_min_f32_e32 v53, v53, v54
	v_max_f32_e32 v52, v55, v52
	v_writelane_b32 v255, s9, 45
	v_and_b32_e32 v45, 0xffffff80, v24
	v_and_b32_e32 v44, 0xffffff80, v27
	v_min_f32_e32 v59, v58, v57
	v_min_f32_e32 v54, v53, v52
	v_max_f32_e32 v57, v58, v57
	v_max_f32_e32 v52, v53, v52
	v_pk_add_f32 v[44:45], v[48:49], v[44:45] op_sel_hi:[0,1]
	v_and_b32_e32 v47, 0xffffff80, v26
	v_min_f32_e32 v58, v57, v52
	v_max_f32_e32 v57, v57, v52
	v_cmp_gt_i32_e32 vcc, 0, v45
	v_mov_b32_e32 v52, 0xf7
	v_and_b32_e32 v46, 0xffffff80, v25
	v_cndmask_b32_e64 v52, v52, 8, vcc
	v_and_or_b32 v45, v45, s12, v52
	v_cmp_gt_i32_e32 vcc, 0, v44
	v_mov_b32_e32 v52, 0xf4
	v_pk_add_f32 v[46:47], v[48:49], v[46:47] op_sel_hi:[0,1]
	v_cndmask_b32_e64 v52, v52, 11, vcc
	v_cmp_gt_i32_e32 vcc, 0, v47
	v_mov_b32_e32 v53, 0xf5
	v_min_f32_e32 v55, v59, v54
	v_max_f32_e32 v59, v59, v54
	v_cndmask_b32_e64 v53, v53, 10, vcc
	v_cmp_gt_i32_e32 vcc, 0, v46
	v_mov_b32_e32 v54, 0xf6
	v_and_b32_e32 v47, 0xffffff00, v47
	v_cndmask_b32_e64 v54, v54, 9, vcc
	v_and_b32_e32 v46, 0xffffff00, v46
	v_and_b32_e32 v44, 0xffffff00, v44
	v_or_b32_e32 v47, v53, v47
	v_or_b32_e32 v46, v54, v46
	v_or_b32_e32 v44, v52, v44
	v_and_b32_e32 v51, 0xffffff80, v29
	v_and_b32_e32 v50, 0xffffff80, v28
	v_writelane_b32 v255, s11, 46
	v_min_f32_e32 v52, v47, v44
	v_max_f32_e32 v53, v45, v46
	v_min_f32_e32 v46, v45, v46
	v_max_f32_e32 v47, v47, v44
	v_pk_add_f32 v[44:45], v[48:49], v[50:51] op_sel_hi:[0,1]
	v_cmp_gt_i32_e64 s[10:11], 0, v45
	v_mov_b32_e32 v50, 0xf2
	v_mov_b32_e32 v51, 0xf3
	v_cndmask_b32_e64 v50, v50, 13, s[10:11]
	v_cmp_gt_i32_e64 s[10:11], 0, v44
	v_and_b32_e32 v45, 0xffffff00, v45
	v_and_b32_e32 v44, 0xffffff00, v44
	v_cndmask_b32_e64 v51, v51, 12, s[10:11]
	v_or_b32_e32 v50, v50, v45
	v_or_b32_e32 v51, v51, v44
	v_and_b32_e32 v45, 0xffffff80, v31
	v_mov_b32_e32 v44, v49
	v_pk_add_f32 v[44:45], v[48:49], v[44:45] op_sel_hi:[0,1]
	v_cmp_gt_i32_e64 s[42:43], 0, v45
	v_mov_b32_e32 v249, 0xf0
	v_mov_b32_e32 v173, 0xf1
	v_cndmask_b32_e64 v63, v249, 15, s[42:43]
	v_cmp_gt_i32_e64 s[42:43], 0, v44
	v_and_b32_e32 v45, 0xffffff00, v45
	v_and_b32_e32 v44, 0xffffff00, v44
	v_cndmask_b32_e64 v173, v173, 14, s[42:43]
	v_or_b32_e32 v45, v63, v45
	v_or_b32_e32 v44, v173, v44
	v_max_f32_e32 v62, v51, v50
	v_min_f32_e32 v63, v44, v45
	v_min_f32_e32 v50, v51, v50
	v_max_f32_e32 v44, v44, v45
	v_max_f32_e32 v54, v53, v52
	v_max_f32_e32 v60, v46, v47
	v_min_f32_e32 v173, v62, v63
	v_min_f32_e32 v45, v50, v44
	v_min_f32_e32 v51, v53, v52
	v_min_f32_e32 v46, v46, v47
	v_max_f32_e32 v52, v62, v63
	v_max_f32_e32 v44, v50, v44
	v_max_f32_e32 v61, v54, v60
	v_min_f32_e32 v178, v173, v45
	v_max_f32_e32 v47, v51, v46
	v_min_f32_e32 v50, v52, v44
	v_min_f32_e32 v54, v54, v60
	v_max_f32_e32 v45, v173, v45
	v_min_f32_e32 v46, v51, v46
	v_max_f32_e32 v44, v52, v44
	v_min_f32_e32 v179, v61, v178
	v_min_f32_e32 v53, v47, v50
	v_min_f32_e32 v60, v54, v45
	v_min_f32_e32 v52, v46, v44
	v_max_f32_e32 v61, v61, v178
	v_max_f32_e32 v47, v47, v50
	v_max_f32_e32 v45, v54, v45
	v_max_f32_e32 v44, v46, v44
	v_min_f32_e32 v62, v179, v53
	v_min_f32_e32 v63, v60, v52
	v_min_f32_e32 v50, v61, v47
	v_min_f32_e32 v46, v45, v44
	v_max_f32_e32 v53, v179, v53
	v_max_f32_e32 v52, v60, v52
	v_max_f32_e32 v47, v61, v47
	v_max_f32_e32 v44, v45, v44
	v_min_f32_e32 v60, v53, v52
	v_min_f32_e32 v61, v47, v44
	v_max_f32_e32 v52, v53, v52
	v_max_f32_e32 v53, v47, v44
	v_and_b32_e32 v44, 0xffffff80, v1
	v_add_f32_e32 v45, v39, v44
	v_min_f32_e32 v51, v62, v63
	v_min_f32_e32 v173, v50, v46
	v_max_f32_e32 v62, v62, v63
	v_max_f32_e32 v63, v50, v46
	v_cmp_gt_i32_e32 vcc, 0, v45
	v_mov_b32_e32 v46, 0xec
	v_mov_b32_e32 v47, 0xe9
	v_cndmask_b32_e64 v46, v46, 19, vcc
	v_and_or_b32 v45, v45, s12, v46
	v_pk_add_f32 v[42:43], v[44:45], v[42:43] op_sel_hi:[0,1]
	v_cmp_gt_i32_e32 vcc, 0, v43
	v_mov_b32_e32 v46, 0xeb
	v_pk_add_f32 v[40:41], v[44:45], v[40:41] op_sel_hi:[0,1]
	v_cndmask_b32_e64 v46, v46, 20, vcc
	v_and_or_b32 v43, v43, s12, v46
	v_cmp_gt_i32_e32 vcc, 0, v42
	v_mov_b32_e32 v46, 0xe8
	v_mov_b32_e32 v50, 0xea
	v_cndmask_b32_e64 v46, v46, 23, vcc
	v_cmp_gt_i32_e32 vcc, 0, v41
	v_and_b32_e32 v41, 0xffffff00, v41
	v_and_b32_e32 v42, 0xffffff00, v42
	v_cndmask_b32_e64 v47, v47, 22, vcc
	v_cmp_gt_i32_e32 vcc, 0, v40
	v_and_b32_e32 v40, 0xffffff00, v40
	v_or_b32_e32 v41, v47, v41
	v_cndmask_b32_e64 v50, v50, 21, vcc
	v_or_b32_e32 v40, v50, v40
	v_or_b32_e32 v42, v46, v42
	v_and_b32_e32 v182, 0xffffff80, v3
	v_min_f32_e32 v46, v41, v42
	v_max_f32_e32 v47, v43, v40
	v_min_f32_e32 v40, v43, v40
	v_max_f32_e32 v41, v41, v42
	v_and_b32_e32 v37, 0xffffff80, v4
	v_max_f32_e32 v43, v47, v46
	v_min_f32_e32 v42, v40, v41
	v_max_f32_e32 v40, v40, v41
	v_min_f32_e32 v50, v47, v46
	v_and_b32_e32 v46, 0xffffff80, v2
	v_and_b32_e32 v36, 0xffffff80, v18
	v_min_f32_e32 v179, v43, v40
	v_max_f32_e32 v180, v43, v40
	v_pk_add_f32 v[40:41], v[46:47], v[38:39] op_sel_hi:[0,1]
	v_cmp_gt_i32_e32 vcc, 0, v41
	v_mov_b32_e32 v38, 0xdc
	v_and_b32_e32 v35, 0xffffff80, v7
	v_cndmask_b32_e64 v38, v38, 35, vcc
	v_and_or_b32 v41, v41, s12, v38
	v_cmp_gt_i32_e32 vcc, 0, v40
	v_mov_b32_e32 v38, 0xdb
	v_and_b32_e32 v34, 0xffffff80, v17
	v_cndmask_b32_e64 v38, v38, 36, vcc
	v_and_or_b32 v181, v40, s12, v38
	v_add_f32_e32 v38, v39, v182
	v_cmp_gt_i32_e32 vcc, 0, v38
	v_mov_b32_e32 v39, 0xcc
	s_nop 0
	v_cndmask_b32_e64 v39, v39, 51, vcc
	v_and_or_b32 v54, v38, s12, v39
	v_pk_add_f32 v[38:39], v[48:49], v[36:37]
	v_min_f32_e32 v178, v50, v42
	v_cmp_gt_i32_e32 vcc, 0, v38
	v_bfrev_b32_e32 v39, -0.5
	v_max_f32_e32 v50, v50, v42
	v_cndmask_b32_e64 v39, v39, 2, vcc
	v_and_or_b32 v38, v38, s12, v39
	v_mov_b32_e32 v39, 0xed
	v_and_b32_e32 v43, 0xffffff80, v6
	v_min_f32_e32 v183, v38, v56
	v_max_f32_e32 v56, v38, v56
	v_add_f32_e32 v38, v36, v44
	v_cmp_gt_i32_e32 vcc, 0, v38
	v_and_b32_e32 v42, 0xffffff80, v5
	v_and_b32_e32 v33, 0xffffff80, v14
	v_cndmask_b32_e64 v39, v39, 18, vcc
	v_and_or_b32 v38, v38, s12, v39
	v_mov_b32_e32 v39, 0xdd
	v_and_b32_e32 v32, 0xffffff80, v16
	v_min_f32_e32 v190, v38, v45
	v_max_f32_e32 v195, v38, v45
	v_add_f32_e32 v38, v36, v46
	v_cmp_gt_i32_e32 vcc, 0, v38
	v_mov_b32_e32 v45, 0x61
	v_mov_b32_e32 v234, 0xef
	v_cndmask_b32_e64 v39, v39, 34, vcc
	v_and_or_b32 v38, v38, s12, v39
	v_mov_b32_e32 v39, 0xcd
	v_mov_b32_e32 v241, 0xdf
	v_min_f32_e32 v209, v38, v41
	v_max_f32_e32 v210, v38, v41
	v_add_f32_e32 v38, v36, v182
	v_cmp_gt_i32_e32 vcc, 0, v38
	v_mov_b32_e32 v41, 0x42
	v_mov_b32_e32 v244, 0xcf
	v_cndmask_b32_e64 v39, v39, 50, vcc
	v_and_or_b32 v40, v38, s12, v39
	v_pk_add_f32 v[38:39], v[36:37], v[36:37] op_sel:[1,0] op_sel_hi:[0,1]
	v_cmp_gt_i32_e32 vcc, 0, v38
	v_mov_b32_e32 v39, 0xbd
	v_and_b32_e32 v47, 0xffffff80, v8
	v_cndmask_b32_e32 v39, v39, v41, vcc
	v_and_or_b32 v41, v38, s12, v39
	v_pk_add_f32 v[38:39], v[48:49], v[34:35]
	v_pk_add_f32 v[48:49], v[48:49], v[32:33]
	v_cmp_gt_i32_e32 vcc, 0, v38
	v_mov_b32_e32 v39, 0xfe
	s_mov_b32 s28, 0xff61b1e6
	v_cndmask_b32_e64 v39, v39, 1, vcc
	v_and_or_b32 v211, v38, s12, v39
	v_add_f32_e32 v38, v34, v44
	v_cmp_gt_i32_e32 vcc, 0, v38
	v_mov_b32_e32 v39, 0xee
	v_add_f32_e32 v44, v32, v44
	v_cndmask_b32_e64 v39, v39, 17, vcc
	v_and_or_b32 v212, v38, s12, v39
	v_add_f32_e32 v38, v34, v46
	v_cmp_gt_i32_e32 vcc, 0, v38
	v_mov_b32_e32 v39, 0xde
	v_add_f32_e32 v46, v32, v46
	v_cndmask_b32_e64 v39, v39, 33, vcc
	v_and_or_b32 v213, v38, s12, v39
	v_add_f32_e32 v38, v34, v182
	v_cmp_gt_i32_e32 vcc, 0, v38
	v_mov_b32_e32 v39, 0xce
	v_add_f32_e32 v182, v32, v182
	v_cndmask_b32_e64 v39, v39, 49, vcc
	v_and_or_b32 v38, v38, s12, v39
	v_cmp_gt_i32_e64 s[74:75], 0, v46
	v_cmp_gt_i32_e64 s[84:85], 0, v182
	v_min_f32_e32 v219, v38, v40
	v_max_f32_e32 v220, v38, v40
	v_pk_add_f32 v[38:39], v[36:37], v[34:35] op_sel:[1,0] op_sel_hi:[0,1]
	v_cmp_gt_i32_e32 vcc, 0, v38
	v_mov_b32_e32 v39, 0xbe
	v_mov_b32_e32 v40, 0x41
	v_cndmask_b32_e32 v39, v39, v40, vcc
	v_and_or_b32 v38, v38, s12, v39
	v_mov_b32_e32 v40, v35
	v_cndmask_b32_e64 v241, v241, 32, s[74:75]
	v_min_f32_e32 v215, v38, v41
	v_max_f32_e32 v216, v38, v41
	v_pk_add_f32 v[38:39], v[34:35], v[42:43]
	v_mov_b32_e32 v41, v43
	v_pk_add_f32 v[40:41], v[34:35], v[40:41] op_sel_hi:[0,1]
	v_cmp_gt_i32_e32 vcc, 0, v38
	v_mov_b32_e32 v34, 0xae
	v_mov_b32_e32 v39, 0x51
	v_cndmask_b32_e32 v34, v34, v39, vcc
	v_cmp_gt_i32_e32 vcc, 0, v41
	v_mov_b32_e32 v39, 0x9e
	v_and_b32_e32 v38, 0xffffff00, v38
	v_cndmask_b32_e32 v39, v39, v45, vcc
	v_or_b32_e32 v218, v34, v38
	v_cmp_gt_i32_e32 vcc, 0, v40
	v_mov_b32_e32 v34, 0x8e
	v_mov_b32_e32 v38, 0x71
	v_cndmask_b32_e32 v34, v34, v38, vcc
	v_and_or_b32 v214, v40, s12, v34
	v_cmp_gt_i32_e32 vcc, 0, v48
	v_mov_b32_e32 v34, 0xff
	v_cndmask_b32_e64 v244, v244, 48, s[84:85]
	v_cndmask_b32_e64 v34, v34, 0, vcc
	v_and_or_b32 v34, v48, s12, v34
	v_and_or_b32 v46, v46, s12, v241
	v_and_or_b32 v182, v182, s12, v244
	v_max_f32_e32 v48, v34, v211
	v_min_f32_e32 v34, v34, v211
	v_max_f32_e32 v49, v48, v183
	v_max_f32_e32 v211, v34, v56
	v_min_f32_e32 v48, v48, v183
	v_min_f32_e32 v34, v34, v56
	v_max_f32_e32 v221, v49, v211
	v_max_f32_e32 v56, v48, v34
	v_min_f32_e32 v49, v49, v211
	v_min_f32_e32 v34, v48, v34
	v_max_f32_e32 v222, v221, v55
	v_max_f32_e32 v183, v56, v58
	v_max_f32_e32 v211, v49, v59
	v_max_f32_e32 v48, v34, v57
	v_min_f32_e32 v55, v221, v55
	v_min_f32_e32 v56, v56, v58
	v_min_f32_e32 v49, v49, v59
	v_min_f32_e32 v34, v34, v57
	v_max_f32_e32 v241, v46, v213
	v_max_f32_e32 v58, v55, v56
	v_max_f32_e32 v57, v49, v34
	v_min_f32_e32 v55, v55, v56
	v_min_f32_e32 v34, v49, v34
	v_min_f32_e32 v46, v46, v213
	v_max_f32_e32 v244, v181, v182
	v_max_f32_e32 v49, v55, v34
	v_min_f32_e32 v34, v55, v34
	v_cmp_gt_i32_e64 s[6:7], 0, v44
	v_min_f32_e32 v181, v181, v182
	s_nop 0
	v_cndmask_b32_e64 v234, v234, 16, s[6:7]
	v_and_or_b32 v44, v44, s12, v234
	v_max_f32_e32 v234, v44, v212
	v_min_f32_e32 v44, v44, v212
	v_max_f32_e32 v235, v234, v190
	v_max_f32_e32 v212, v44, v195
	v_min_f32_e32 v190, v234, v190
	v_min_f32_e32 v44, v44, v195
	v_max_f32_e32 v242, v241, v209
	v_max_f32_e32 v213, v46, v210
	v_min_f32_e32 v245, v244, v219
	v_min_f32_e32 v182, v181, v220
	v_min_f32_e32 v209, v241, v209
	v_min_f32_e32 v46, v46, v210
	v_max_f32_e32 v219, v244, v219
	v_max_f32_e32 v181, v181, v220
	v_max_f32_e32 v59, v58, v57
	v_min_f32_e32 v57, v58, v57
	v_max_f32_e32 v236, v235, v212
	v_max_f32_e32 v195, v190, v44
	v_min_f32_e32 v212, v235, v212
	v_min_f32_e32 v44, v190, v44
	v_max_f32_e32 v243, v242, v213
	v_min_f32_e32 v246, v245, v182
	v_max_f32_e32 v210, v209, v46
	v_min_f32_e32 v220, v219, v181
	v_min_f32_e32 v213, v242, v213
	v_max_f32_e32 v182, v245, v182
	v_min_f32_e32 v46, v209, v46
	v_max_f32_e32 v181, v219, v181
	v_max_f32_e32 v237, v236, v178
	v_max_f32_e32 v234, v195, v179
	v_max_f32_e32 v235, v212, v50
	v_max_f32_e32 v190, v44, v180
	v_min_f32_e32 v247, v243, v246
	v_min_f32_e32 v241, v210, v220
	v_min_f32_e32 v242, v213, v182
	v_min_f32_e32 v209, v46, v181
	v_min_f32_e32 v178, v236, v178
	v_min_f32_e32 v179, v195, v179
	v_min_f32_e32 v50, v212, v50
	v_min_f32_e32 v44, v44, v180
	v_max_f32_e32 v236, v243, v246
	v_max_f32_e32 v210, v210, v220
	v_max_f32_e32 v182, v213, v182
	v_max_f32_e32 v46, v46, v181
	v_max_f32_e32 v223, v222, v183
	v_max_f32_e32 v224, v211, v48
	v_min_f32_e32 v183, v222, v183
	v_min_f32_e32 v48, v211, v48
	v_max_f32_e32 v238, v237, v234
	v_max_f32_e32 v239, v235, v190
	v_min_f32_e32 v244, v247, v241
	v_min_f32_e32 v219, v242, v209
	v_max_f32_e32 v195, v178, v179
	v_max_f32_e32 v180, v50, v44
	v_min_f32_e32 v220, v236, v210
	v_min_f32_e32 v181, v182, v46
	v_min_f32_e32 v234, v237, v234
	v_min_f32_e32 v190, v235, v190
	v_max_f32_e32 v237, v247, v241
	v_max_f32_e32 v209, v242, v209
	v_min_f32_e32 v178, v178, v179
	v_min_f32_e32 v44, v50, v44
	v_max_f32_e32 v50, v236, v210
	v_max_f32_e32 v46, v182, v46
	v_max_f32_e32 v225, v223, v224
	v_max_f32_e32 v211, v183, v48
	v_min_f32_e32 v223, v223, v224
	v_min_f32_e32 v48, v183, v48
	v_max_f32_e32 v240, v238, v239
	v_min_f32_e32 v245, v244, v219
	v_max_f32_e32 v212, v195, v180
	v_min_f32_e32 v213, v220, v181
	v_max_f32_e32 v235, v234, v190
	v_min_f32_e32 v241, v237, v209
	v_max_f32_e32 v179, v178, v44
	v_min_f32_e32 v182, v50, v46
	v_min_f32_e32 v238, v238, v239
	v_max_f32_e32 v219, v244, v219
	v_min_f32_e32 v180, v195, v180
	v_max_f32_e32 v181, v220, v181
	v_min_f32_e32 v190, v234, v190
	v_max_f32_e32 v209, v237, v209
	v_min_f32_e32 v44, v178, v44
	v_max_f32_e32 v46, v50, v46
	v_max_f32_e32 v226, v225, v51
	v_max_f32_e32 v221, v59, v173
	v_max_f32_e32 v222, v211, v60
	v_max_f32_e32 v56, v49, v61
	v_max_f32_e32 v224, v223, v62
	v_max_f32_e32 v58, v57, v63
	v_max_f32_e32 v183, v48, v52
	v_max_f32_e32 v55, v34, v53
	v_min_f32_e32 v248, v240, v245
	v_min_f32_e32 v243, v212, v213
	v_min_f32_e32 v242, v235, v241
	v_min_f32_e32 v210, v179, v182
	v_min_f32_e32 v239, v238, v219
	v_min_f32_e32 v195, v180, v181
	v_min_f32_e32 v234, v190, v209
	v_min_f32_e32 v178, v44, v46
	v_max_f32_e32 v227, v226, v221
	v_max_f32_e32 v228, v222, v56
	v_max_f32_e32 v230, v224, v58
	v_max_f32_e32 v231, v183, v55
	v_min_f32_e32 v246, v248, v243
	v_min_f32_e32 v236, v242, v210
	v_min_f32_e32 v220, v239, v195
	v_min_f32_e32 v237, v234, v178
	v_max_f32_e32 v229, v227, v228
	v_max_f32_e32 v232, v230, v231
	v_min_f32_e32 v247, v246, v236
	v_min_f32_e32 v244, v220, v237
	v_min_f32_e32 v51, v225, v51
	v_min_f32_e32 v59, v59, v173
	v_min_f32_e32 v60, v211, v60
	v_min_f32_e32 v61, v49, v61
	v_min_f32_e32 v62, v223, v62
	v_min_f32_e32 v57, v57, v63
	v_min_f32_e32 v48, v48, v52
	v_min_f32_e32 v34, v34, v53
	v_max_f32_e32 v63, v240, v245
	v_max_f32_e32 v212, v212, v213
	v_max_f32_e32 v235, v235, v241
	v_max_f32_e32 v179, v179, v182
	v_max_f32_e32 v219, v238, v219
	v_max_f32_e32 v180, v180, v181
	v_max_f32_e32 v190, v190, v209
	v_max_f32_e32 v44, v44, v46
	v_max_f32_e32 v233, v229, v232
	v_min_f32_e32 v50, v247, v244
	v_max_f32_e32 v173, v51, v59
	v_max_f32_e32 v211, v60, v61
	v_max_f32_e32 v223, v62, v57
	v_max_f32_e32 v53, v48, v34
	v_min_f32_e32 v213, v63, v212
	v_min_f32_e32 v182, v235, v179
	v_min_f32_e32 v181, v219, v180
	v_min_f32_e32 v46, v190, v44
	v_min_f32_e32 v227, v227, v228
	v_min_f32_e32 v228, v230, v231
	v_max_f32_e32 v230, v246, v236
	v_max_f32_e32 v220, v220, v237
	v_max_f32_e32 v50, v233, v50
	v_max_f32_e32 v44, v190, v44
	v_max_f32_e32 v225, v173, v211
	v_max_f32_e32 v233, v223, v53
	v_min_f32_e32 v240, v213, v182
	v_min_f32_e32 v209, v181, v46
	v_min_f32_e32 v221, v226, v221
	v_min_f32_e32 v222, v222, v56
	v_min_f32_e32 v224, v224, v58
	v_min_f32_e32 v183, v183, v55
	v_max_f32_e32 v241, v248, v243
	v_max_f32_e32 v210, v242, v210
	v_max_f32_e32 v195, v239, v195
	v_max_f32_e32 v234, v234, v178
	v_min_f32_e32 v51, v51, v59
	v_min_f32_e32 v59, v60, v61
	v_min_f32_e32 v57, v62, v57
	v_min_f32_e32 v34, v48, v34
	v_max_f32_e32 v60, v63, v212
	v_max_f32_e32 v62, v235, v179
	v_max_f32_e32 v58, v227, v228
	v_min_f32_e32 v63, v230, v220
	v_min_f32_e32 v211, v173, v211
	v_min_f32_e32 v223, v223, v53
	v_max_f32_e32 v213, v213, v182
	v_max_f32_e32 v46, v181, v46
	v_max_f32_e32 v226, v221, v222
	v_max_f32_e32 v238, v224, v183
	v_max_f32_e32 v243, v51, v59
	v_max_f32_e32 v245, v57, v34
	v_min_f32_e32 v179, v60, v62
	v_max_f32_e32 v63, v58, v63
	v_max_f32_e32 v53, v211, v223
	v_min_f32_e32 v58, v213, v46
	v_min_f32_e32 v181, v221, v222
	v_min_f32_e32 v221, v224, v183
	v_max_f32_e32 v222, v241, v210
	v_max_f32_e32 v224, v195, v234
	v_min_f32_e32 v51, v51, v59
	v_min_f32_e32 v59, v57, v34
	v_max_f32_e32 v231, v60, v62
	v_min_f32_e32 v57, v229, v232
	v_max_f32_e32 v62, v247, v244
	v_min_f32_e32 v239, v195, v234
	v_min_f32_e32 v242, v241, v210
	v_max_f32_e32 v212, v219, v180
	v_max_f32_e32 v178, v53, v58
	v_max_f32_e32 v53, v181, v221
	v_min_f32_e32 v173, v222, v224
	v_max_f32_e32 v183, v57, v62
	v_min_f32_e32 v57, v225, v233
	v_max_f32_e32 v62, v240, v209
	v_min_f32_e32 v219, v212, v44
	v_max_f32_e32 v180, v53, v173
	v_max_f32_e32 v190, v57, v62
	v_min_f32_e32 v57, v226, v238
	v_max_f32_e32 v173, v242, v239
	v_max_f32_e32 v55, v226, v238
	v_min_f32_e32 v56, v242, v239
	v_max_f32_e32 v210, v230, v220
	v_max_f32_e32 v195, v57, v173
	v_min_f32_e32 v57, v243, v245
	v_max_f32_e32 v173, v179, v219
	v_max_f32_e32 v55, v55, v56
	v_min_f32_e32 v56, v179, v219
	v_min_f32_e32 v179, v227, v228
	v_min_f32_e32 v52, v240, v209
	v_max_f32_e32 v209, v57, v173
	v_max_f32_e32 v46, v213, v46
	v_max_f32_e32 v44, v212, v44
	v_max_f32_e32 v210, v179, v210
	v_min_f32_e32 v179, v211, v223
	v_max_f32_e32 v211, v179, v46
	v_min_f32_e32 v46, v181, v221
	v_max_f32_e32 v181, v222, v224
	v_min_f32_e32 v53, v231, v44
	v_max_f32_e32 v44, v231, v44
	v_max_f32_e32 v212, v46, v181
	v_min_f32_e32 v46, v51, v59
	v_max_f32_e32 v34, v51, v59
	v_pk_add_f32 v[36:37], v[36:37], v[32:33] op_sel:[1,0] op_sel_hi:[0,1]
	v_mov_b32_e32 v37, 0xbf
	v_max_f32_e32 v213, v46, v44
	v_cmp_gt_i32_e32 vcc, 0, v36
	v_mov_b32_e32 v221, 0x50
	v_and_b32_e32 v41, 0xffffff00, v41
	v_cndmask_b32_e64 v37, v37, 64, vcc
	v_and_or_b32 v36, v36, s12, v37
	v_or_b32_e32 v217, v39, v41
	v_max_f32_e32 v49, v225, v233
	v_max_f32_e32 v44, v54, v36
	v_min_f32_e32 v54, v54, v36
	v_pk_add_f32 v[36:37], v[32:33], v[42:43] op_sel_hi:[0,1]
	v_cmp_gt_i32_e64 s[68:69], 0, v37
	v_mov_b32_e32 v42, 0x9f
	v_mov_b32_e32 v43, 0x60
	v_cndmask_b32_e64 v42, v42, v43, s[68:69]
	v_cmp_gt_i32_e64 s[68:69], 0, v36
	v_mov_b32_e32 v43, 0xaf
	v_and_b32_e32 v37, 0xffffff00, v37
	v_cndmask_b32_e64 v43, v43, v221, s[68:69]
	v_and_b32_e32 v36, 0xffffff00, v36
	v_or_b32_e32 v37, v42, v37
	v_or_b32_e32 v36, v43, v36
	v_min_f32_e32 v42, v37, v217
	v_max_f32_e32 v43, v36, v218
	v_max_f32_e32 v37, v37, v217
	v_min_f32_e32 v36, v36, v218
	v_max_f32_e32 v46, v44, v215
	v_max_f32_e32 v219, v54, v216
	v_min_f32_e32 v221, v43, v42
	v_min_f32_e32 v217, v36, v37
	v_max_f32_e32 v42, v43, v42
	v_max_f32_e32 v36, v36, v37
	v_max_f32_e32 v220, v46, v219
	v_min_f32_e32 v44, v44, v215
	v_min_f32_e32 v54, v54, v216
	v_min_f32_e32 v219, v46, v219
	v_mov_b32_e32 v46, v35
	v_min_f32_e32 v216, v42, v36
	v_max_f32_e32 v225, v42, v36
	v_pk_add_f32 v[36:37], v[32:33], v[46:47] op_sel_hi:[0,1]
	v_and_b32_e32 v45, 0xffffff80, v9
	v_max_f32_e32 v215, v44, v54
	v_min_f32_e32 v54, v44, v54
	v_mov_b32_e32 v44, v35
	v_cmp_gt_i32_e32 vcc, 0, v37
	v_mov_b32_e32 v35, 0x7f
	v_pk_add_f32 v[42:43], v[32:33], v[44:45] op_sel_hi:[0,1]
	v_cndmask_b32_e32 v35, v35, v196, vcc
	v_cmp_gt_i32_e32 vcc, 0, v36
	v_mov_b32_e32 v47, 0x8f
	v_mov_b32_e32 v45, 0x6f
	v_cndmask_b32_e32 v44, v47, v198, vcc
	v_cmp_gt_i32_e32 vcc, 0, v43
	v_mov_b32_e32 v46, 0x90
	v_and_b32_e32 v37, 0xffffff00, v37
	v_and_b32_e32 v36, 0xffffff00, v36
	v_cndmask_b32_e32 v45, v45, v46, vcc
	v_and_b32_e32 v43, 0xffffff00, v43
	v_cmp_gt_i32_e32 vcc, 0, v42
	v_or_b32_e32 v35, v35, v37
	v_or_b32_e32 v36, v44, v36
	v_or_b32_e32 v37, v45, v43
	v_and_b32_e32 v41, 0xffffff80, v10
	v_and_b32_e32 v40, 0xffffff80, v13
	v_cndmask_b32_e32 v46, v47, v198, vcc
	v_cmp_lt_f32_e32 vcc, v37, v35
	v_cmp_lt_f32_e64 s[8:9], v214, v36
	v_and_b32_e32 v39, 0xffffff80, v12
	v_cndmask_b32_e32 v43, v35, v37, vcc
	v_cndmask_b32_e64 v45, v36, v214, s[8:9]
	v_cndmask_b32_e32 v35, v37, v35, vcc
	v_pk_add_f32 v[36:37], v[32:33], v[40:41] op_sel_hi:[0,1]
	v_cmp_gt_i32_e64 s[80:81], 0, v37
	v_mov_b32_e32 v40, 0x5f
	v_mov_b32_e32 v41, 0xa0
	v_and_b32_e32 v38, 0xffffff80, v11
	v_cndmask_b32_e64 v40, v40, v41, s[80:81]
	v_and_b32_e32 v42, 0xffffff00, v42
	v_and_or_b32 v37, v37, s12, v40
	v_cmp_gt_i32_e64 s[80:81], 0, v36
	v_mov_b32_e32 v40, 0xd0
	v_pk_add_f32 v[38:39], v[32:33], v[38:39] op_sel_hi:[0,1]
	v_or_b32_e32 v42, v46, v42
	v_cndmask_b32_e64 v40, 47, v40, s[80:81]
	v_cmp_gt_i32_e64 s[80:81], 0, v39
	v_mov_b32_e32 v41, 0xc0
	v_cndmask_b32_e64 v42, v214, v42, s[8:9]
	v_cndmask_b32_e64 v41, 63, v41, s[80:81]
	v_cmp_gt_i32_e64 s[80:81], 0, v38
	v_mov_b32_e32 v214, 0x4f
	v_mov_b32_e32 v229, 0xb0
	v_cndmask_b32_e64 v214, v214, v229, s[80:81]
	v_and_b32_e32 v39, 0xffffff00, v39
	v_and_b32_e32 v38, 0xffffff00, v38
	v_and_b32_e32 v36, 0xffffff00, v36
	v_or_b32_e32 v39, v41, v39
	v_or_b32_e32 v38, v214, v38
	v_or_b32_e32 v36, v40, v36
	v_min_f32_e32 v40, v39, v36
	v_max_f32_e32 v41, v37, v38
	v_min_f32_e32 v37, v37, v38
	v_max_f32_e32 v36, v39, v36
	v_max_f32_e32 v44, v42, v43
	v_max_f32_e32 v46, v45, v35
	v_min_f32_e32 v214, v41, v40
	v_min_f32_e32 v38, v37, v36
	v_min_f32_e32 v42, v42, v43
	v_min_f32_e32 v35, v45, v35
	v_max_f32_e32 v40, v41, v40
	v_max_f32_e32 v36, v37, v36
	v_max_f32_e32 v47, v44, v46
	v_min_f32_e32 v39, v214, v38
	v_max_f32_e32 v43, v42, v35
	v_min_f32_e32 v37, v40, v36
	v_min_f32_e32 v44, v44, v46
	v_max_f32_e32 v38, v214, v38
	v_min_f32_e32 v35, v42, v35
	v_max_f32_e32 v36, v40, v36
	v_min_f32_e32 v218, v221, v217
	v_max_f32_e32 v217, v221, v217
	v_min_f32_e32 v229, v47, v39
	v_min_f32_e32 v41, v43, v37
	v_min_f32_e32 v46, v44, v38
	v_min_f32_e32 v40, v35, v36
	v_max_f32_e32 v39, v47, v39
	v_max_f32_e32 v37, v43, v37
	v_max_f32_e32 v38, v44, v38
	v_max_f32_e32 v35, v35, v36
	v_max_f32_e32 v222, v220, v218
	v_max_f32_e32 v223, v215, v216
	v_max_f32_e32 v221, v219, v217
	v_max_f32_e32 v226, v54, v225
	v_min_f32_e32 v218, v220, v218
	v_min_f32_e32 v215, v215, v216
	v_min_f32_e32 v217, v219, v217
	v_min_f32_e32 v54, v54, v225
	v_min_f32_e32 v43, v39, v37
	v_min_f32_e32 v36, v38, v35
	v_max_f32_e32 v37, v39, v37
	v_max_f32_e32 v35, v38, v35
	v_max_f32_e32 v216, v218, v215
	v_max_f32_e32 v219, v217, v54
	v_min_f32_e32 v44, v43, v36
	v_min_f32_e32 v215, v218, v215
	v_min_f32_e32 v54, v217, v54
	v_min_f32_e32 v38, v37, v35
	v_max_f32_e32 v43, v43, v36
	v_max_f32_e32 v35, v37, v35
	v_and_b32_e32 v37, 0xffffff80, v15
	v_mov_b32_e32 v36, v33
	v_pk_add_f32 v[32:33], v[32:33], v[36:37] op_sel_hi:[0,1]
	v_mov_b32_e32 v37, 0xe0
	v_max_f32_e32 v217, v215, v54
	v_min_f32_e32 v54, v215, v54
	v_cmp_gt_i32_e64 s[76:77], 0, v33
	v_and_b32_e32 v33, 0xffffff00, v33
	s_nop 0
	v_cndmask_b32_e64 v36, 15, v249, s[76:77]
	v_cmp_gt_i32_e64 s[76:77], 0, v32
	v_and_b32_e32 v32, 0xffffff00, v32
	v_or_b32_e32 v33, v36, v33
	v_cndmask_b32_e64 v37, 31, v37, s[76:77]
	v_or_b32_e32 v32, v37, v32
	v_max_f32_e32 v36, v32, v33
	v_min_f32_e32 v32, v32, v33
	v_max_f32_e32 v37, v36, v36
	v_max_f32_e32 v33, v32, v32
	v_max_f32_e32 v37, 0xff61b1e6, v37
	v_max_f32_e32 v33, 0xff61b1e6, v33
	v_max_f32_e32 v224, v222, v223
	v_max_f32_e32 v233, v37, v33
	v_min_f32_e32 v33, v37, v33
	v_max_f32_e32 v234, 0xff61b1e6, v233
	v_max_f32_e32 v37, 0xff61b1e6, v33
	v_cmp_nlt_f32_e32 vcc, s28, v33
	v_max_f32_e32 v227, v221, v226
	v_max_f32_e32 v235, v234, v37
	v_cmp_nlt_f32_e64 s[88:89], s28, v235
	v_cndmask_b32_e32 v33, v199, v33, vcc
	v_min_f32_e32 v45, v229, v41
	v_cndmask_b32_e64 v236, v199, v235, s[88:89]
	v_cmp_nlt_f32_e64 s[88:89], s28, v233
	v_min_f32_e32 v42, v46, v40
	v_min_f32_e32 v222, v222, v223
	v_cndmask_b32_e64 v233, v199, v233, s[88:89]
	v_cmp_nlt_f32_e64 s[88:89], s28, v36
	v_min_f32_e32 v221, v221, v226
	v_max_f32_e32 v41, v229, v41
	v_cndmask_b32_e64 v36, v199, v36, s[88:89]
	v_cmp_nlt_f32_e64 s[88:89], s28, v32
	v_max_f32_e32 v40, v46, v40
	s_nop 0
	v_cndmask_b32_e64 v32, v199, v32, s[88:89]
	v_max_f32_e32 v237, v36, v32
	v_min_f32_e32 v32, v36, v32
	v_max_f32_e32 v238, v233, v237
	v_max_f32_e32 v36, v33, v32
	v_max_f32_e32 v228, v224, v227
	v_min_f32_e32 v214, v45, v42
	v_max_f32_e32 v220, v216, v219
	v_max_f32_e32 v223, v222, v221
	v_min_f32_e32 v46, v41, v40
	v_min_f32_e32 v224, v224, v227
	v_max_f32_e32 v42, v45, v42
	v_min_f32_e32 v216, v216, v219
	v_min_f32_e32 v221, v222, v221
	v_max_f32_e32 v40, v41, v40
	v_max_f32_e32 v239, v238, v36
	v_min_f32_e32 v233, v233, v237
	v_min_f32_e32 v32, v33, v32
	v_min_f32_e32 v37, v234, v37
	v_min_f32_e32 v36, v238, v36
	v_max_f32_e32 v52, v49, v52
	s_mov_b64 s[6:7], s[96:97]
	v_cmp_nlt_f32_e64 s[88:89], s28, v239
	v_cmp_nlt_f32_e64 s[76:77], s28, v37
	v_cmp_nlt_f32_e64 s[14:15], s28, v36
	v_max_f32_e32 v230, v228, v214
	v_max_f32_e32 v47, v220, v44
	v_max_f32_e32 v226, v223, v46
	v_max_f32_e32 v39, v217, v38
	v_max_f32_e32 v45, v224, v42
	v_max_f32_e32 v219, v216, v43
	v_max_f32_e32 v41, v221, v40
	v_max_f32_e32 v215, v54, v35
	v_cndmask_b32_e64 v240, v199, v239, s[88:89]
	v_max_f32_e32 v33, v233, v32
	v_cndmask_b32_e64 v234, v199, v37, s[76:77]
	v_cndmask_b32_e64 v238, v199, v36, s[14:15]
	v_min_f32_e32 v32, v233, v32
	v_cmp_nlt_f32_e64 s[88:89], s28, v33
	v_cmp_nlt_f32_e32 vcc, s28, v32
	v_max_f32_e32 v48, v243, v245
	v_max_f32_e32 v225, v230, v47
	v_max_f32_e32 v218, v226, v39
	v_max_f32_e32 v227, v45, v219
	v_max_f32_e32 v222, v41, v215
	v_min_f32_e32 v241, v236, v240
	v_cndmask_b32_e64 v237, v199, v33, s[88:89]
	v_min_f32_e32 v243, v234, v238
	v_cndmask_b32_e32 v233, v199, v32, vcc
	v_max_f32_e32 v229, v225, v218
	v_max_f32_e32 v231, v227, v222
	v_min_f32_e32 v242, v241, v237
	v_min_f32_e32 v244, v243, v233
	v_min_f32_e32 v214, v228, v214
	v_max_f32_e32 v232, v229, v231
	v_min_f32_e32 v245, v242, v244
	v_max_f32_e32 v228, 0xff61b1e6, v235
	v_max_f32_e32 v235, v239, v239
	v_max_f32_e32 v36, v36, v36
	v_min_f32_e32 v44, v220, v44
	v_min_f32_e32 v46, v223, v46
	v_min_f32_e32 v38, v217, v38
	v_min_f32_e32 v42, v224, v42
	v_min_f32_e32 v43, v216, v43
	v_min_f32_e32 v40, v221, v40
	v_min_f32_e32 v35, v54, v35
	v_max_f32_e32 v235, 0xff61b1e6, v235
	v_max_f32_e32 v33, v33, v33
	v_max_f32_e32 v37, 0xff61b1e6, v37
	v_max_f32_e32 v36, 0xff61b1e6, v36
	v_max_f32_e32 v32, v32, v32
	v_max_f32_e32 v232, v232, v245
	s_mov_b32 s36, s18
	v_max_f32_e32 v33, 0xff61b1e6, v33
	v_max_f32_e32 v32, 0xff61b1e6, v32
	v_max_f32_e32 v220, v214, v44
	v_max_f32_e32 v217, v46, v38
	v_max_f32_e32 v216, v42, v43
	v_max_f32_e32 v54, v40, v35
	v_min_f32_e32 v239, v228, v235
	v_min_f32_e32 v245, 0xff61b1e6, v33
	v_min_f32_e32 v247, v37, v36
	v_min_f32_e32 v248, 0xff61b1e6, v32
	v_max_f32_e32 v223, v220, v217
	v_max_f32_e32 v221, v216, v54
	v_min_f32_e32 v246, v239, v245
	v_min_f32_e32 v249, v247, v248
	v_min_f32_e32 v47, v230, v47
	v_max_f32_e32 v230, v236, v240
	v_cmp_ngt_f32_e64 s[16:17], s28, v237
	v_max_f32_e32 v234, v234, v238
	v_cmp_ngt_f32_e64 s[14:15], s28, v233
	v_min_f32_e32 v44, v214, v44
	v_min_f32_e32 v38, v46, v38
	v_min_f32_e32 v42, v42, v43
	v_min_f32_e32 v35, v40, v35
	v_max_f32_e32 v214, v228, v235
	v_max_f32_e32 v36, v37, v36
	v_max_f32_e32 v224, v223, v221
	v_min_f32_e32 v250, v246, v249
	v_min_f32_e32 v39, v226, v39
	v_min_f32_e32 v45, v45, v219
	v_min_f32_e32 v41, v41, v215
	v_cndmask_b32_e64 v236, v199, v237, s[16:17]
	v_cndmask_b32_e64 v238, v199, v233, s[14:15]
	v_max_f32_e32 v46, v44, v38
	v_max_f32_e32 v40, v42, v35
	v_min_f32_e32 v228, v214, v33
	v_min_f32_e32 v37, v36, v32
	v_max_f32_e32 v224, v224, v250
	v_max_f32_e32 v226, v47, v39
	v_max_f32_e32 v215, v45, v41
	v_min_f32_e32 v240, v230, v236
	v_min_f32_e32 v250, v234, v238
	v_min_f32_e32 v218, v225, v218
	v_min_f32_e32 v222, v227, v222
	v_max_f32_e32 v237, v241, v237
	v_max_f32_e32 v233, v243, v233
	v_min_f32_e32 v39, v47, v39
	v_min_f32_e32 v41, v45, v41
	v_max_f32_e32 v47, v230, v236
	v_max_f32_e32 v230, v234, v238
	v_max_f32_e32 v43, v46, v40
	v_min_f32_e32 v235, v228, v37
	v_min_f32_e32 v217, v220, v217
	v_min_f32_e32 v54, v216, v54
	v_max_f32_e32 v239, v239, v245
	v_max_f32_e32 v243, v247, v248
	v_min_f32_e32 v38, v44, v38
	v_min_f32_e32 v35, v42, v35
	v_max_f32_e32 v33, v214, v33
	v_max_f32_e32 v32, v36, v32
	v_max_f32_e32 v219, v226, v215
	v_max_f32_e32 v227, v218, v222
	v_min_f32_e32 v241, v237, v233
	v_max_f32_e32 v45, v39, v41
	v_min_f32_e32 v234, v47, v230
	v_min_f32_e32 v229, v229, v231
	v_max_f32_e32 v231, v242, v244
	v_min_f32_e32 v215, v226, v215
	v_max_f32_e32 v226, v240, v250
	v_min_f32_e32 v251, v240, v250
	v_max_f32_e32 v43, v43, v235
	v_max_f32_e32 v216, v217, v54
	v_min_f32_e32 v245, v239, v243
	v_max_f32_e32 v42, v38, v35
	v_min_f32_e32 v36, v33, v32
	v_min_f32_e32 v221, v223, v221
	v_max_f32_e32 v223, v246, v249
	v_min_f32_e32 v40, v46, v40
	v_max_f32_e32 v37, v228, v37
	v_min_f32_e32 v218, v218, v222
	v_max_f32_e32 v222, v237, v233
	v_min_f32_e32 v54, v217, v54
	v_max_f32_e32 v217, v239, v243
	v_min_f32_e32 v39, v39, v41
	v_max_f32_e32 v41, v47, v230
	v_min_f32_e32 v35, v38, v35
	v_max_f32_e32 v32, v33, v32
	v_max_f32_e32 v227, v227, v241
	v_max_f32_e32 v45, v45, v234
	v_max_f32_e32 v229, v229, v231
	v_max_f32_e32 v215, v215, v226
	v_max_f32_e32 v61, v48, v56
	v_max_f32_e32 v182, v34, v53
	v_max_f32_e32 v219, v219, v251
	v_max_f32_e32 v216, v216, v245
	v_max_f32_e32 v36, v42, v36
	v_max_f32_e32 v221, v221, v223
	v_max_f32_e32 v37, v40, v37
	v_max_f32_e32 v218, v218, v222
	v_max_f32_e32 v217, v54, v217
	v_max_f32_e32 v39, v39, v41
	v_max_f32_e32 v32, v35, v32
	v_max_f32_e32 v49, v50, v52
	v_max_f32_e32 v56, v55, v61
	v_max_f32_e32 v58, v63, v178
	v_max_f32_e32 v60, v180, v182
	v_max_f32_e32 v62, v183, v190
	v_max_f32_e32 v173, v195, v209
	v_max_f32_e32 v179, v210, v211
	v_max_f32_e32 v181, v212, v213
	v_min_f32_e32 v225, v232, v224
	v_min_f32_e32 v241, v219, v43
	v_min_f32_e32 v245, v227, v216
	v_min_f32_e32 v42, v45, v36
	v_min_f32_e32 v223, v229, v221
	v_min_f32_e32 v40, v215, v37
	v_min_f32_e32 v222, v218, v217
	v_min_f32_e32 v33, v39, v32
	v_max_f32_e32 v48, v49, v56
	v_max_f32_e32 v53, v58, v60
	v_max_f32_e32 v57, v62, v173
	v_max_f32_e32 v59, v179, v181
	v_min_f32_e32 v220, v225, v241
	v_min_f32_e32 v44, v245, v42
	v_min_f32_e32 v46, v223, v40
	v_min_f32_e32 v35, v222, v33
	v_max_f32_e32 v34, v48, v53
	v_max_f32_e32 v51, v57, v59
	v_min_f32_e32 v214, v220, v44
	v_min_f32_e32 v38, v46, v35
	v_min_f32_e32 v47, v55, v61
	v_max_f32_e32 v235, v34, v51
	v_min_f32_e32 v41, v214, v38
	v_min_f32_e32 v61, v63, v178
	v_min_f32_e32 v63, v180, v182
	v_max_f32_e32 v54, v235, v41
	v_min_f32_e32 v41, v50, v52
	v_min_f32_e32 v182, v183, v190
	v_min_f32_e32 v183, v195, v209
	v_min_f32_e32 v190, v210, v211
	v_min_f32_e32 v209, v212, v213
	v_max_f32_e32 v212, v232, v224
	v_max_f32_e32 v43, v219, v43
	v_max_f32_e32 v216, v227, v216
	v_max_f32_e32 v36, v45, v36
	v_max_f32_e32 v221, v229, v221
	v_max_f32_e32 v37, v215, v37
	v_max_f32_e32 v217, v218, v217
	v_max_f32_e32 v32, v39, v32
	v_min_f32_e32 v49, v49, v56
	v_min_f32_e32 v224, v58, v60
	v_min_f32_e32 v62, v62, v173
	v_min_f32_e32 v173, v179, v181
	v_max_f32_e32 v181, v225, v241
	v_max_f32_e32 v42, v245, v42
	v_max_f32_e32 v40, v223, v40
	v_max_f32_e32 v33, v222, v33
	v_max_f32_e32 v50, v41, v47
	v_max_f32_e32 v178, v61, v63
	v_max_f32_e32 v195, v182, v183
	v_min_f32_e32 v213, v212, v43
	v_min_f32_e32 v45, v216, v36
	v_min_f32_e32 v215, v221, v37
	v_min_f32_e32 v39, v217, v32
	v_max_f32_e32 v226, v49, v224
	v_max_f32_e32 v179, v62, v173
	v_min_f32_e32 v225, v181, v42
	v_min_f32_e32 v222, v40, v33
	v_min_f32_e32 v41, v41, v47
	v_min_f32_e32 v47, v61, v63
	v_min_f32_e32 v63, v182, v183
	v_min_f32_e32 v182, v190, v209
	v_max_f32_e32 v43, v212, v43
	v_max_f32_e32 v36, v216, v36
	v_max_f32_e32 v37, v221, v37
	v_max_f32_e32 v32, v217, v32
	v_cmp_gt_f32_e64 s[24:25], v63, v182
	v_max_f32_e32 v210, v190, v209
	v_max_f32_e32 v56, v226, v179
	v_min_f32_e32 v58, v225, v222
	v_max_f32_e32 v223, v41, v47
	v_cndmask_b32_e64 v183, v182, v63, s[24:25]
	v_min_f32_e32 v209, v43, v36
	v_min_f32_e32 v212, v37, v32
	v_max_f32_e32 v56, v56, v58
	v_max_f32_e32 v58, v223, v183
	v_min_f32_e32 v60, v209, v212
	v_min_f32_e32 v48, v48, v53
	v_min_f32_e32 v217, v57, v59
	v_max_f32_e32 v44, v220, v44
	v_max_f32_e32 v35, v46, v35
	v_max_f32_e32 v58, v58, v60
	v_max_f32_e32 v53, v48, v217
	v_min_f32_e32 v46, v44, v35
	v_max_f32_e32 v180, v50, v178
	v_min_f32_e32 v219, v213, v45
	v_min_f32_e32 v218, v215, v39
	v_max_f32_e32 v59, v53, v46
	v_min_f32_e32 v46, v50, v178
	v_min_f32_e32 v50, v195, v210
	v_max_f32_e32 v45, v213, v45
	v_max_f32_e32 v39, v215, v39
	v_min_f32_e32 v49, v49, v224
	v_max_f32_e32 v53, v46, v50
	v_min_f32_e32 v57, v45, v39
	v_min_f32_e32 v213, v62, v173
	v_max_f32_e32 v42, v181, v42
	v_max_f32_e32 v33, v40, v33
	v_max_f32_e32 v60, v53, v57
	v_cmp_gt_f32_e64 s[20:21], v49, v213
	v_max_f32_e32 v211, v195, v210
	s_nop 0
	v_cndmask_b32_e64 v57, v213, v49, s[20:21]
	v_min_f32_e32 v40, v42, v33
	v_max_f32_e32 v36, v43, v36
	v_max_f32_e32 v32, v37, v32
	v_max_f32_e32 v61, v57, v40
	v_min_f32_e32 v40, v41, v47
	v_cndmask_b32_e64 v41, v63, v182, s[24:25]
	v_cmp_gt_f32_e64 s[14:15], v40, v41
	v_min_f32_e32 v34, v34, v51
	s_nop 0
	v_cndmask_b32_e64 v47, v41, v40, s[14:15]
	v_min_f32_e32 v37, v36, v32
	s_mov_b64 s[96:97], s[6:7]
	v_max_f32_e32 v62, v47, v37
	v_max_f32_e32 v37, v214, v38
	v_max_f32_e32 v35, v44, v35
	v_min_f32_e32 v55, v219, v218
	v_max_f32_e32 v63, v34, v37
	v_min_f32_e32 v34, v180, v211
	v_max_f32_e32 v37, v219, v218
	v_max_f32_e32 v52, v180, v211
	v_max_f32_e32 v33, v42, v33
	v_max_f32_e32 v173, v34, v37
	v_min_f32_e32 v34, v226, v179
	v_max_f32_e32 v37, v225, v222
	v_max_f32_e32 v32, v36, v32
	v_max_f32_e32 v178, v34, v37
	v_min_f32_e32 v34, v223, v183
	v_max_f32_e32 v37, v209, v212
	v_max_f32_e32 v55, v52, v55
	v_max_f32_e32 v179, v34, v37
	v_min_f32_e32 v34, v48, v217
	v_max_f32_e32 v180, v34, v35
	v_min_f32_e32 v34, v46, v50
	v_max_f32_e32 v35, v45, v39
	v_max_f32_e32 v181, v34, v35
	v_cndmask_b32_e64 v34, v49, v213, s[20:21]
	v_max_f32_e32 v182, v34, v33
	v_cndmask_b32_e64 v33, v40, v41, s[14:15]
	v_min_f32_e32 v52, v54, v55
	v_min_f32_e32 v190, v56, v58
	v_max_f32_e32 v183, v33, v32
	v_min_f32_e32 v53, v59, v60
	v_min_f32_e32 v57, v61, v62
	v_min_f32_e32 v195, v63, v173
	v_min_f32_e32 v209, v178, v179
	v_min_f32_e32 v210, v180, v181
	v_min_f32_e32 v211, v182, v183
	v_min_f32_e32 v216, v52, v190
	v_min_f32_e32 v215, v53, v57
	v_min_f32_e32 v51, v195, v209
	v_min_f32_e32 v50, v210, v211
	s_movk_i32 s10, 0xff
	v_min_f32_e32 v220, v216, v215
	v_min_f32_e32 v212, v51, v50
	s_movk_i32 s8, 0x7f
	v_bitop3_b32 v35, v31, s8, v31 bitop3:0xc
	v_min_f32_e32 v32, v220, v212
	v_and_b32_e32 v33, 0xff, v32
	v_bitop3_b32 v34, v32, s10, v32 bitop3:0xc
	v_cmp_gt_i32_e64 s[6:7], 0, v32
	v_readlane_b32 s94, v255, 39
	v_readlane_b32 s95, v255, 40
	v_cndmask_b32_e64 v213, v34, v33, s[6:7]
	v_and_b32_e32 v33, 0x7f, v31
	v_cmp_gt_i32_e64 s[6:7], 0, v31
	v_and_b32_e32 v34, 15, v213
	v_lshrrev_b32_e32 v214, 4, v213
	v_cndmask_b32_e64 v31, v35, v33, s[6:7]
	v_and_b32_e32 v33, 0x7f, v30
	v_bitop3_b32 v35, v30, s8, v30 bitop3:0xc
	v_cmp_gt_i32_e64 s[6:7], 0, v30
	v_readlane_b32 s86, v255, 31
	v_readlane_b32 s82, v255, 33
	v_cndmask_b32_e64 v30, v35, v33, s[6:7]
	v_and_b32_e32 v33, 0x7f, v29
	v_bitop3_b32 v35, v29, s8, v29 bitop3:0xc
	v_cmp_gt_i32_e64 s[6:7], 0, v29
	v_readlane_b32 s84, v255, 25
	v_readlane_b32 s87, v255, 32
	v_cndmask_b32_e64 v29, v35, v33, s[6:7]
	v_and_b32_e32 v33, 0x7f, v28
	v_bitop3_b32 v35, v28, s8, v28 bitop3:0xc
	v_cmp_gt_i32_e64 s[6:7], 0, v28
	v_readlane_b32 s92, v255, 35
	v_readlane_b32 s88, v255, 29
	v_cndmask_b32_e64 v28, v35, v33, s[6:7]
	v_and_b32_e32 v33, 0x7f, v27
	v_bitop3_b32 v35, v27, s8, v27 bitop3:0xc
	v_cmp_gt_i32_e64 s[6:7], 0, v27
	v_readlane_b32 s90, v255, 27
	v_readlane_b32 s78, v255, 13
	v_cndmask_b32_e64 v27, v35, v33, s[6:7]
	v_and_b32_e32 v33, 0x7f, v26
	v_bitop3_b32 v35, v26, s8, v26 bitop3:0xc
	v_cmp_gt_i32_e64 s[6:7], 0, v26
	v_readlane_b32 s83, v255, 34
	v_readlane_b32 s74, v255, 9
	v_cndmask_b32_e64 v26, v35, v33, s[6:7]
	v_and_b32_e32 v33, 0x7f, v25
	v_bitop3_b32 v35, v25, s8, v25 bitop3:0xc
	v_cmp_gt_i32_e64 s[6:7], 0, v25
	v_readlane_b32 s85, v255, 26
	v_readlane_b32 s76, v255, 11
	v_cndmask_b32_e64 v25, v35, v33, s[6:7]
	v_and_b32_e32 v33, 0x7f, v24
	v_bitop3_b32 v35, v24, s8, v24 bitop3:0xc
	v_cmp_gt_i32_e64 s[6:7], 0, v24
	v_readlane_b32 s22, v255, 23
	v_readlane_b32 s34, v255, 17
	v_cndmask_b32_e64 v24, v35, v33, s[6:7]
	v_and_b32_e32 v33, 0x7f, v23
	v_bitop3_b32 v35, v23, s8, v23 bitop3:0xc
	v_cmp_gt_i32_e64 s[6:7], 0, v23
	v_readlane_b32 s30, v255, 15
	v_readlane_b32 s81, v255, 41
	v_cndmask_b32_e64 v23, v35, v33, s[6:7]
	v_and_b32_e32 v33, 0x7f, v22
	v_bitop3_b32 v35, v22, s8, v22 bitop3:0xc
	v_cmp_gt_i32_e64 s[6:7], 0, v22
	s_movk_i32 s87, 0x4000
	v_readlane_b32 s93, v255, 36
	v_cndmask_b32_e64 v22, v35, v33, s[6:7]
	v_and_b32_e32 v33, 0x7f, v21
	v_bitop3_b32 v35, v21, s8, v21 bitop3:0xc
	v_cmp_gt_i32_e64 s[6:7], 0, v21
	v_readlane_b32 s89, v255, 30
	v_readlane_b32 s91, v255, 28
	v_cndmask_b32_e64 v21, v35, v33, s[6:7]
	v_and_b32_e32 v33, 0x7f, v20
	v_bitop3_b32 v35, v20, s8, v20 bitop3:0xc
	v_cmp_gt_i32_e64 s[6:7], 0, v20
	v_readlane_b32 s79, v255, 14
	v_readlane_b32 s83, v255, 37
	v_cndmask_b32_e64 v20, v35, v33, s[6:7]
	v_and_b32_e32 v33, 0x7f, v19
	v_bitop3_b32 v35, v19, s8, v19 bitop3:0xc
	v_cmp_gt_i32_e64 s[6:7], 0, v19
	v_readlane_b32 s75, v255, 10
	v_readlane_b32 s85, v255, 38
	v_cndmask_b32_e64 v19, v35, v33, s[6:7]
	v_and_b32_e32 v33, 0x7f, v18
	v_bitop3_b32 v35, v18, s8, v18 bitop3:0xc
	v_cmp_gt_i32_e64 s[6:7], 0, v18
	v_readlane_b32 s77, v255, 12
	v_readlane_b32 s23, v255, 24
	v_cndmask_b32_e64 v18, v35, v33, s[6:7]
	v_and_b32_e32 v33, 0x7f, v17
	v_bitop3_b32 v35, v17, s8, v17 bitop3:0xc
	v_cmp_gt_i32_e64 s[6:7], 0, v17
	s_mov_b32 s18, s36
	s_movk_i32 s27, 0x1200
	v_cndmask_b32_e64 v17, v35, v33, s[6:7]
	v_and_b32_e32 v33, 0x7f, v16
	v_bitop3_b32 v35, v16, s8, v16 bitop3:0xc
	v_cmp_gt_i32_e64 s[6:7], 0, v16
	v_readlane_b32 s35, v255, 18
	v_readlane_b32 s31, v255, 16
	v_cndmask_b32_e64 v33, v35, v33, s[6:7]
	v_lshl_add_u32 v252, v34, 8, v207
	ds_read_b32 v16, v252 offset:4096
	v_bitop3_b32 v35, v15, s8, v15 bitop3:0xc
	s_nop 0
	s_nop 1
	s_nop 1
	s_nop 1
	s_nop 1
	s_nop 1
	s_nop 1
	s_nop 1
	s_nop 1
	s_nop 1
	s_nop 1
	s_nop 1
	s_nop 1
	s_nop 1
	s_nop 1
	v_and_b32_e32 v34, 0x7f, v15
	s_nop 0
	s_waitcnt lgkmcnt(0)
	v_and_b32_e32 v252, 0x7f, v16
	v_cmp_gt_i32_e64 s[6:7], 0, v16
	v_xor_b32_e32 v16, 0x7f, v252
	s_nop 0
	v_cndmask_b32_e64 v16, v16, v252, s[6:7]
	v_cmp_gt_i32_e64 s[6:7], 0, v15
	v_and_b32_e32 v15, 0x7f, v14
	s_nop 0
	v_cndmask_b32_e64 v34, v35, v34, s[6:7]
	v_bitop3_b32 v35, v14, s8, v14 bitop3:0xc
	v_cmp_gt_i32_e64 s[6:7], 0, v14
	v_and_b32_e32 v14, 0x7f, v13
	s_nop 0
	v_cndmask_b32_e64 v35, v35, v15, s[6:7]
	v_bitop3_b32 v15, v13, s8, v13 bitop3:0xc
	v_cmp_gt_i32_e64 s[6:7], 0, v13
	v_and_b32_e32 v13, 0x7f, v12
	s_nop 0
	v_cndmask_b32_e64 v36, v15, v14, s[6:7]
	v_bitop3_b32 v14, v12, s8, v12 bitop3:0xc
	v_cmp_gt_i32_e64 s[6:7], 0, v12
	v_and_b32_e32 v12, 0x7f, v11
	v_max_f32_e32 v15, v59, v60
	v_cndmask_b32_e64 v37, v14, v13, s[6:7]
	v_bitop3_b32 v13, v11, s8, v11 bitop3:0xc
	v_cmp_gt_i32_e64 s[6:7], 0, v11
	v_and_b32_e32 v11, 0x7f, v10
	v_max_f32_e32 v14, v56, v58
	v_cndmask_b32_e64 v38, v13, v12, s[6:7]
	v_bitop3_b32 v12, v10, s8, v10 bitop3:0xc
	v_cmp_gt_i32_e64 s[6:7], 0, v10
	v_and_b32_e32 v10, 0x7f, v9
	v_max_f32_e32 v59, v61, v62
	v_cndmask_b32_e64 v39, v12, v11, s[6:7]
	v_bitop3_b32 v11, v9, s8, v9 bitop3:0xc
	v_cmp_gt_i32_e64 s[6:7], 0, v9
	v_and_b32_e32 v9, 0x7f, v8
	v_max_f32_e32 v60, v63, v173
	v_cndmask_b32_e64 v40, v11, v10, s[6:7]
	v_bitop3_b32 v10, v8, s8, v8 bitop3:0xc
	v_cmp_gt_i32_e64 s[6:7], 0, v8
	v_and_b32_e32 v8, 0x7f, v7
	v_max_f32_e32 v61, v178, v179
	v_cndmask_b32_e64 v41, v10, v9, s[6:7]
	v_bitop3_b32 v9, v7, s8, v7 bitop3:0xc
	v_cmp_gt_i32_e64 s[6:7], 0, v7
	v_and_b32_e32 v7, 0x7f, v6
	v_max_f32_e32 v62, v180, v181
	v_cndmask_b32_e64 v42, v9, v8, s[6:7]
	v_bitop3_b32 v8, v6, s8, v6 bitop3:0xc
	v_cmp_gt_i32_e64 s[6:7], 0, v6
	v_and_b32_e32 v6, 0x7f, v5
	v_max_f32_e32 v9, v210, v211
	v_cndmask_b32_e64 v43, v8, v7, s[6:7]
	v_bitop3_b32 v7, v5, s8, v5 bitop3:0xc
	v_cmp_gt_i32_e64 s[6:7], 0, v5
	v_and_b32_e32 v5, 0x7f, v4
	v_max_f32_e32 v8, v195, v209
	v_cndmask_b32_e64 v44, v7, v6, s[6:7]
	v_bitop3_b32 v6, v4, s8, v4 bitop3:0xc
	v_cmp_gt_i32_e64 s[6:7], 0, v4
	v_and_b32_e32 v4, 0x7f, v3
	v_max_f32_e32 v63, v182, v183
	v_cndmask_b32_e64 v45, v6, v5, s[6:7]
	v_bitop3_b32 v5, v3, s8, v3 bitop3:0xc
	v_cmp_gt_i32_e64 s[6:7], 0, v3
	v_and_b32_e32 v3, 0x7f, v2
	s_nop 0
	v_cndmask_b32_e64 v46, v5, v4, s[6:7]
	v_bitop3_b32 v4, v2, s8, v2 bitop3:0xc
	v_cmp_gt_i32_e64 s[6:7], 0, v2
	v_and_b32_e32 v2, 0x7f, v1
	s_nop 0
	v_cndmask_b32_e64 v47, v4, v3, s[6:7]
	v_bitop3_b32 v3, v1, s8, v1 bitop3:0xc
	v_cmp_gt_i32_e64 s[6:7], 0, v1
	v_and_b32_e32 v1, 0x7f, v0
	v_max_f32_e32 v4, v51, v50
	v_cndmask_b32_e64 v48, v3, v2, s[6:7]
	v_bitop3_b32 v2, v0, s8, v0 bitop3:0xc
	v_cmp_gt_i32_e64 s[6:7], 0, v0
	v_min_f32_e32 v56, v60, v61
	s_nop 0
	v_cndmask_b32_e64 v49, v2, v1, s[6:7]
	v_lshl_add_u32 v252, v214, 8, v207
	ds_read_b32 v0, v252
	v_min_f32_e32 v58, v62, v63
	s_nop 0
	v_max_f32_e32 v60, v60, v61
	v_max_f32_e32 v61, v62, v63
	v_readlane_b32 s46, v255, 21
	v_readlane_b32 s44, v255, 19
	v_readlane_b32 s47, v255, 22
	v_readlane_b32 s45, v255, 20
	s_nop 1
	s_nop 1
	s_nop 1
	s_nop 1
	s_nop 1
	s_nop 1
	s_nop 1
	s_nop 1
	s_nop 1
	s_nop 1
	s_nop 1
	s_nop 1
	s_waitcnt lgkmcnt(0)
	v_and_b32_e32 v252, 0x7f, v0
	v_cmp_gt_i32_e64 s[6:7], 0, v0
	v_xor_b32_e32 v0, 0x7f, v252
	s_nop 0
	v_cndmask_b32_e64 v3, v0, v252, s[6:7]
	v_max_f32_e32 v0, v220, v212
	v_and_b32_e32 v1, 0xff, v0
	v_bitop3_b32 v2, v0, s10, v0 bitop3:0xc
	v_cmp_gt_i32_e64 s[6:7], 0, v0
	v_and_b32_e32 v12, 0xffffff00, v0
	v_lshl_add_u32 v3, v3, 7, v16
	v_cndmask_b32_e64 v0, v2, v1, s[6:7]
	v_lshrrev_b32_e32 v1, 4, v0
	v_lshl_add_u32 v252, v1, 8, v207
	ds_read_b32 v2, v252
	v_and_b32_e32 v0, 15, v0
	s_nop 0
	s_nop 1
	s_nop 1
	s_nop 1
	s_nop 1
	s_nop 1
	s_nop 1
	s_nop 1
	s_nop 1
	s_nop 1
	s_nop 1
	s_nop 1
	s_nop 1
	s_nop 1
	s_nop 1
	s_nop 1
	s_waitcnt lgkmcnt(0)
	v_and_b32_e32 v252, 0x7f, v2
	v_cmp_gt_i32_e64 s[6:7], 0, v2
	v_xor_b32_e32 v2, 0x7f, v252
	s_nop 0
	v_cndmask_b32_e64 v1, v2, v252, s[6:7]
	v_lshl_add_u32 v252, v0, 8, v207
	ds_read_b32 v2, v252 offset:4096
	s_nop 1
	s_nop 1
	s_nop 1
	s_nop 1
	s_nop 1
	s_nop 1
	s_nop 1
	s_nop 1
	s_nop 1
	s_nop 1
	s_nop 1
	s_nop 1
	s_nop 1
	s_nop 1
	s_nop 1
	s_nop 1
	s_waitcnt lgkmcnt(0)
	v_and_b32_e32 v252, 0x7f, v2
	v_cmp_gt_i32_e64 s[6:7], 0, v2
	v_xor_b32_e32 v2, 0x7f, v252
	s_nop 0
	v_cndmask_b32_e64 v0, v2, v252, s[6:7]
	v_lshl_add_u32 v2, v1, 7, v0
	v_max_f32_e32 v0, v216, v215
	v_min_f32_e32 v1, v0, v4
	v_and_b32_e32 v5, 0xff, v1
	v_bitop3_b32 v6, v1, s10, v1 bitop3:0xc
	v_cmp_gt_i32_e64 s[8:9], 0, v1
	v_and_b32_e32 v50, 0xffffff00, v1
	v_max_f32_e32 v0, v0, v4
	v_cndmask_b32_e64 v1, v6, v5, s[8:9]
	v_lshrrev_b32_e32 v5, 4, v1
	v_lshl_add_u32 v252, v5, 8, v207
	ds_read_b32 v6, v252
	v_and_b32_e32 v1, 15, v1
	v_and_b32_e32 v4, 0xff, v0
	v_cmp_gt_i32_e64 s[6:7], 0, v0
	v_and_b32_e32 v51, 0xffffff00, v0
	s_nop 1
	s_nop 1
	s_nop 1
	s_nop 1
	s_nop 1
	s_nop 1
	s_nop 1
	s_nop 1
	s_nop 1
	s_nop 1
	s_nop 1
	s_nop 1
	s_nop 1
	s_nop 1
	s_waitcnt lgkmcnt(0)
	v_and_b32_e32 v252, 0x7f, v6
	v_cmp_gt_i32_e64 s[8:9], 0, v6
	v_xor_b32_e32 v6, 0x7f, v252
	s_nop 0
	v_cndmask_b32_e64 v5, v6, v252, s[8:9]
	v_lshl_add_u32 v252, v1, 8, v207
	ds_read_b32 v6, v252 offset:4096
	s_nop 1
	s_nop 1
	s_nop 1
	s_nop 1
	s_nop 1
	s_nop 1
	s_nop 1
	s_nop 1
	s_nop 1
	s_nop 1
	s_nop 1
	s_nop 1
	s_nop 1
	s_nop 1
	s_nop 1
	s_nop 1
	s_waitcnt lgkmcnt(0)
	v_and_b32_e32 v252, 0x7f, v6
	v_cmp_gt_i32_e64 s[8:9], 0, v6
	v_xor_b32_e32 v6, 0x7f, v252
	s_nop 0
	v_cndmask_b32_e64 v1, v6, v252, s[8:9]
	v_lshl_add_u32 v1, v5, 7, v1
	v_bitop3_b32 v5, v0, s10, v0 bitop3:0xc
	v_cndmask_b32_e64 v0, v5, v4, s[6:7]
	v_lshrrev_b32_e32 v4, 4, v0
	v_lshl_add_u32 v252, v4, 8, v207
	ds_read_b32 v5, v252
	v_and_b32_e32 v0, 15, v0
	s_nop 0
	s_nop 1
	s_nop 1
	s_nop 1
	s_nop 1
	s_nop 1
	s_nop 1
	s_nop 1
	s_nop 1
	s_nop 1
	s_nop 1
	s_nop 1
	s_nop 1
	s_nop 1
	s_nop 1
	s_nop 1
	s_waitcnt lgkmcnt(0)
	v_and_b32_e32 v252, 0x7f, v5
	v_cmp_gt_i32_e64 s[6:7], 0, v5
	v_xor_b32_e32 v5, 0x7f, v252
	s_nop 0
	v_cndmask_b32_e64 v4, v5, v252, s[6:7]
	v_lshl_add_u32 v252, v0, 8, v207
	ds_read_b32 v5, v252 offset:4096
	s_nop 1
	s_nop 1
	s_nop 1
	s_nop 1
	s_nop 1
	s_nop 1
	s_nop 1
	s_nop 1
	s_nop 1
	s_nop 1
	s_nop 1
	s_nop 1
	s_nop 1
	s_nop 1
	s_nop 1
	s_nop 1
	s_waitcnt lgkmcnt(0)
	v_and_b32_e32 v252, 0x7f, v5
	v_cmp_gt_i32_e64 s[6:7], 0, v5
	v_xor_b32_e32 v5, 0x7f, v252
	s_nop 0
	v_cndmask_b32_e64 v0, v5, v252, s[6:7]
	v_lshl_add_u32 v0, v4, 7, v0
	v_max_f32_e32 v4, v52, v190
	v_max_f32_e32 v5, v53, v57
	v_min_f32_e32 v6, v4, v5
	v_min_f32_e32 v10, v8, v9
	v_max_f32_e32 v4, v4, v5
	v_max_f32_e32 v8, v8, v9
	v_min_f32_e32 v7, v6, v10
	v_and_b32_e32 v11, 0xff, v7
	v_bitop3_b32 v13, v7, s10, v7 bitop3:0xc
	v_cmp_gt_i32_e64 s[8:9], 0, v7
	v_and_b32_e32 v52, 0xffffff00, v7
	v_max_f32_e32 v6, v6, v10
	v_cndmask_b32_e64 v7, v13, v11, s[8:9]
	v_lshrrev_b32_e32 v11, 4, v7
	v_lshl_add_u32 v252, v11, 8, v207
	ds_read_b32 v13, v252
	v_and_b32_e32 v7, 15, v7
	v_and_b32_e32 v10, 0xff, v6
	v_cmp_gt_i32_e64 s[6:7], 0, v6
	v_and_b32_e32 v53, 0xffffff00, v6
	s_nop 1
	s_nop 1
	s_nop 1
	s_nop 1
	s_nop 1
	s_nop 1
	s_nop 1
	s_nop 1
	s_nop 1
	s_nop 1
	s_nop 1
	s_nop 1
	s_nop 1
	s_nop 1
	s_waitcnt lgkmcnt(0)
	v_and_b32_e32 v252, 0x7f, v13
	v_cmp_gt_i32_e64 s[8:9], 0, v13
	v_xor_b32_e32 v13, 0x7f, v252
	s_nop 0
	v_cndmask_b32_e64 v11, v13, v252, s[8:9]
	v_lshl_add_u32 v252, v7, 8, v207
	ds_read_b32 v13, v252 offset:4096
	s_nop 1
	s_nop 1
	s_nop 1
	s_nop 1
	s_nop 1
	s_nop 1
	s_nop 1
	s_nop 1
	s_nop 1
	s_nop 1
	s_nop 1
	s_nop 1
	s_nop 1
	s_nop 1
	s_nop 1
	s_nop 1
	s_waitcnt lgkmcnt(0)
	v_and_b32_e32 v252, 0x7f, v13
	v_cmp_gt_i32_e64 s[8:9], 0, v13
	v_xor_b32_e32 v13, 0x7f, v252
	s_nop 0
	v_cndmask_b32_e64 v7, v13, v252, s[8:9]
	v_lshl_add_u32 v7, v11, 7, v7
	v_bitop3_b32 v11, v6, s10, v6 bitop3:0xc
	v_cndmask_b32_e64 v6, v11, v10, s[6:7]
	v_lshrrev_b32_e32 v10, 4, v6
	v_lshl_add_u32 v252, v10, 8, v207
	ds_read_b32 v11, v252
	v_and_b32_e32 v6, 15, v6
	v_max_f32_e32 v13, v54, v55
	v_min_f32_e32 v55, v56, v58
	s_nop 0
	v_max_f32_e32 v58, v56, v58
	s_nop 0
	s_nop 1
	s_nop 1
	s_nop 1
	s_nop 1
	s_nop 1
	s_nop 1
	s_nop 1
	s_nop 1
	s_nop 1
	s_nop 1
	s_nop 1
	s_nop 1
	s_nop 1
	s_waitcnt lgkmcnt(0)
	v_and_b32_e32 v252, 0x7f, v11
	v_cmp_gt_i32_e64 s[6:7], 0, v11
	v_xor_b32_e32 v11, 0x7f, v252
	s_nop 0
	v_cndmask_b32_e64 v10, v11, v252, s[6:7]
	v_lshl_add_u32 v252, v6, 8, v207
	ds_read_b32 v11, v252 offset:4096
	s_nop 1
	s_nop 1
	s_nop 1
	s_nop 1
	s_nop 1
	s_nop 1
	s_nop 1
	s_nop 1
	s_nop 1
	s_nop 1
	s_nop 1
	s_nop 1
	s_nop 1
	s_nop 1
	s_nop 1
	s_nop 1
	s_waitcnt lgkmcnt(0)
	v_and_b32_e32 v252, 0x7f, v11
	v_cmp_gt_i32_e64 s[6:7], 0, v11
	v_xor_b32_e32 v11, 0x7f, v252
	s_nop 0
	v_cndmask_b32_e64 v6, v11, v252, s[6:7]
	v_lshl_add_u32 v6, v10, 7, v6
	v_min_f32_e32 v5, v4, v8
	v_and_b32_e32 v9, 0xff, v5
	v_bitop3_b32 v10, v5, s10, v5 bitop3:0xc
	v_cmp_gt_i32_e64 s[8:9], 0, v5
	v_and_b32_e32 v57, 0xffffff00, v5
	v_max_f32_e32 v4, v4, v8
	v_cndmask_b32_e64 v5, v10, v9, s[8:9]
	v_lshrrev_b32_e32 v9, 4, v5
	v_lshl_add_u32 v252, v9, 8, v207
	ds_read_b32 v10, v252
	v_and_b32_e32 v5, 15, v5
	v_and_b32_e32 v8, 0xff, v4
	v_cmp_gt_i32_e64 s[6:7], 0, v4
	v_and_b32_e32 v209, 0xffffff00, v4
	s_nop 1
	s_nop 1
	s_nop 1
	s_nop 1
	s_nop 1
	s_nop 1
	s_nop 1
	s_nop 1
	s_nop 1
	s_nop 1
	s_nop 1
	s_nop 1
	s_nop 1
	s_nop 1
	s_waitcnt lgkmcnt(0)
	v_and_b32_e32 v252, 0x7f, v10
	v_cmp_gt_i32_e64 s[8:9], 0, v10
	v_xor_b32_e32 v10, 0x7f, v252
	s_nop 0
	v_cndmask_b32_e64 v9, v10, v252, s[8:9]
	v_lshl_add_u32 v252, v5, 8, v207
	ds_read_b32 v10, v252 offset:4096
	s_nop 1
	s_nop 1
	s_nop 1
	s_nop 1
	s_nop 1
	s_nop 1
	s_nop 1
	s_nop 1
	s_nop 1
	s_nop 1
	s_nop 1
	s_nop 1
	s_nop 1
	s_nop 1
	s_nop 1
	s_nop 1
	s_waitcnt lgkmcnt(0)
	v_and_b32_e32 v252, 0x7f, v10
	v_cmp_gt_i32_e64 s[8:9], 0, v10
	v_xor_b32_e32 v10, 0x7f, v252
	s_nop 0
	v_cndmask_b32_e64 v5, v10, v252, s[8:9]
	v_lshl_add_u32 v5, v9, 7, v5
	v_bitop3_b32 v9, v4, s10, v4 bitop3:0xc
	v_cndmask_b32_e64 v4, v9, v8, s[6:7]
	v_lshrrev_b32_e32 v8, 4, v4
	v_lshl_add_u32 v252, v8, 8, v207
	ds_read_b32 v9, v252
	v_and_b32_e32 v4, 15, v4
	s_nop 0
	s_nop 1
	s_nop 1
	s_nop 1
	s_nop 1
	s_nop 1
	s_nop 1
	s_nop 1
	s_nop 1
	s_nop 1
	s_nop 1
	s_nop 1
	s_nop 1
	s_nop 1
	s_nop 1
	s_nop 1
	s_waitcnt lgkmcnt(0)
	v_and_b32_e32 v252, 0x7f, v9
	v_cmp_gt_i32_e64 s[6:7], 0, v9
	v_xor_b32_e32 v9, 0x7f, v252
	s_nop 0
	v_cndmask_b32_e64 v8, v9, v252, s[6:7]
	v_lshl_add_u32 v252, v4, 8, v207
	ds_read_b32 v9, v252 offset:4096
	s_nop 1
	s_nop 1
	s_nop 1
	s_nop 1
	s_nop 1
	s_nop 1
	s_nop 1
	s_nop 1
	s_nop 1
	s_nop 1
	s_nop 1
	s_nop 1
	s_nop 1
	s_nop 1
	s_nop 1
	s_nop 1
	s_waitcnt lgkmcnt(0)
	v_and_b32_e32 v252, 0x7f, v9
	v_cmp_gt_i32_e64 s[6:7], 0, v9
	v_xor_b32_e32 v9, 0x7f, v252
	s_nop 0
	v_cndmask_b32_e64 v4, v9, v252, s[6:7]
	v_lshl_add_u32 v4, v8, 7, v4
	v_min_f32_e32 v8, v13, v14
	v_min_f32_e32 v9, v15, v59
	v_max_f32_e32 v13, v13, v14
	v_max_f32_e32 v59, v15, v59
	v_min_f32_e32 v10, v8, v9
	v_max_f32_e32 v8, v8, v9
	v_min_f32_e32 v11, v10, v55
	v_and_b32_e32 v173, 0xff, v11
	v_bitop3_b32 v178, v11, s10, v11 bitop3:0xc
	v_cmp_gt_i32_e64 s[8:9], 0, v11
	v_and_b32_e32 v54, 0xffffff00, v11
	v_max_f32_e32 v10, v10, v55
	v_cndmask_b32_e64 v11, v178, v173, s[8:9]
	v_lshrrev_b32_e32 v173, 4, v11
	v_lshl_add_u32 v252, v173, 8, v207
	ds_read_b32 v178, v252
	v_and_b32_e32 v11, 15, v11
	v_cmp_gt_i32_e64 s[6:7], 0, v10
	v_and_b32_e32 v55, 0xffffff00, v10
	s_nop 0
	v_min_f32_e32 v14, v13, v59
	v_min_f32_e32 v62, v60, v61
	v_max_f32_e32 v59, v13, v59
	v_max_f32_e32 v60, v60, v61
	s_nop 0
	s_nop 0
	v_min_f32_e32 v13, v59, v60
	v_and_b32_e32 v61, 0xffffff00, v13
	v_max_f32_e32 v59, v59, v60
	v_cmp_gt_i32_e32 vcc, 0, v59
	v_and_b32_e32 v60, 0xffffff00, v59
	v_sub_f32_e32 v12, v12, v60
	v_mul_f32_e32 v12, 0x3fb8aa3b, v12
	s_nop 0
	s_nop 1
	s_nop 1
	s_nop 1
	s_nop 1
	s_nop 1
	s_nop 1
	s_nop 1
	s_waitcnt lgkmcnt(0)
	v_and_b32_e32 v252, 0x7f, v178
	v_cmp_gt_i32_e64 s[8:9], 0, v178
	v_xor_b32_e32 v178, 0x7f, v252
	s_nop 0
	v_cndmask_b32_e64 v173, v178, v252, s[8:9]
	v_lshl_add_u32 v252, v11, 8, v207
	ds_read_b32 v178, v252 offset:4096
	s_nop 1
	s_nop 1
	s_nop 1
	s_nop 1
	s_nop 1
	s_nop 1
	s_nop 1
	s_nop 1
	s_nop 1
	s_nop 1
	s_nop 1
	s_nop 1
	s_nop 1
	s_nop 1
	s_nop 1
	s_nop 1
	s_waitcnt lgkmcnt(0)
	v_and_b32_e32 v252, 0x7f, v178
	v_cmp_gt_i32_e64 s[8:9], 0, v178
	v_xor_b32_e32 v178, 0x7f, v252
	s_nop 0
	v_cndmask_b32_e64 v11, v178, v252, s[8:9]
	v_lshl_add_u32 v11, v173, 7, v11
	v_and_b32_e32 v173, 0xff, v10
	v_bitop3_b32 v178, v10, s10, v10 bitop3:0xc
	v_cndmask_b32_e64 v10, v178, v173, s[6:7]
	v_lshrrev_b32_e32 v173, 4, v10
	v_lshl_add_u32 v252, v173, 8, v207
	ds_read_b32 v178, v252
	v_and_b32_e32 v10, 15, v10
	s_nop 0
	s_nop 1
	s_nop 1
	s_nop 1
	s_nop 1
	s_nop 1
	s_nop 1
	s_nop 1
	s_nop 1
	s_nop 1
	s_nop 1
	s_nop 1
	s_nop 1
	s_nop 1
	s_nop 1
	s_nop 1
	s_waitcnt lgkmcnt(0)
	v_and_b32_e32 v252, 0x7f, v178
	v_cmp_gt_i32_e64 s[6:7], 0, v178
	v_xor_b32_e32 v178, 0x7f, v252
	s_nop 0
	v_cndmask_b32_e64 v173, v178, v252, s[6:7]
	v_lshl_add_u32 v252, v10, 8, v207
	ds_read_b32 v178, v252 offset:4096
	s_nop 1
	s_nop 1
	s_nop 1
	s_nop 1
	s_nop 1
	s_nop 1
	s_nop 1
	s_nop 1
	s_nop 1
	s_nop 1
	s_nop 1
	s_nop 1
	s_nop 1
	s_nop 1
	s_nop 1
	s_nop 1
	s_waitcnt lgkmcnt(0)
	v_and_b32_e32 v252, 0x7f, v178
	v_cmp_gt_i32_e64 s[6:7], 0, v178
	v_xor_b32_e32 v178, 0x7f, v252
	s_nop 0
	v_cndmask_b32_e64 v10, v178, v252, s[6:7]
	v_lshl_add_u32 v10, v173, 7, v10
	v_min_f32_e32 v9, v8, v58
	v_and_b32_e32 v173, 0xff, v9
	v_bitop3_b32 v178, v9, s10, v9 bitop3:0xc
	v_cmp_gt_i32_e64 s[8:9], 0, v9
	v_and_b32_e32 v56, 0xffffff00, v9
	v_max_f32_e32 v8, v8, v58
	v_cndmask_b32_e64 v9, v178, v173, s[8:9]
	v_lshrrev_b32_e32 v173, 4, v9
	v_lshl_add_u32 v252, v173, 8, v207
	ds_read_b32 v178, v252
	v_and_b32_e32 v9, 15, v9
	v_cmp_gt_i32_e64 s[6:7], 0, v8
	v_and_b32_e32 v58, 0xffffff00, v8
	s_nop 0
	s_nop 1
	s_nop 1
	s_nop 1
	s_nop 1
	s_nop 1
	s_nop 1
	s_nop 1
	s_nop 1
	s_nop 1
	s_nop 1
	s_nop 1
	s_nop 1
	s_nop 1
	s_nop 1
	s_waitcnt lgkmcnt(0)
	v_and_b32_e32 v252, 0x7f, v178
	v_cmp_gt_i32_e64 s[8:9], 0, v178
	v_xor_b32_e32 v178, 0x7f, v252
	s_nop 0
	v_cndmask_b32_e64 v173, v178, v252, s[8:9]
	v_lshl_add_u32 v252, v9, 8, v207
	ds_read_b32 v178, v252 offset:4096
	s_nop 1
	s_nop 1
	s_nop 1
	s_nop 1
	s_nop 1
	s_nop 1
	s_nop 1
	s_nop 1
	s_nop 1
	s_nop 1
	s_nop 1
	s_nop 1
	s_nop 1
	s_nop 1
	s_nop 1
	s_nop 1
	s_waitcnt lgkmcnt(0)
	v_and_b32_e32 v252, 0x7f, v178
	v_cmp_gt_i32_e64 s[8:9], 0, v178
	v_xor_b32_e32 v178, 0x7f, v252
	s_nop 0
	v_cndmask_b32_e64 v9, v178, v252, s[8:9]
	v_lshl_add_u32 v9, v173, 7, v9
	v_and_b32_e32 v173, 0xff, v8
	v_bitop3_b32 v178, v8, s10, v8 bitop3:0xc
	v_cndmask_b32_e64 v8, v178, v173, s[6:7]
	v_lshrrev_b32_e32 v173, 4, v8
	v_lshl_add_u32 v252, v173, 8, v207
	ds_read_b32 v178, v252
	v_and_b32_e32 v8, 15, v8
	s_nop 0
	s_nop 1
	s_nop 1
	s_nop 1
	s_nop 1
	s_nop 1
	s_nop 1
	s_nop 1
	s_nop 1
	s_nop 1
	s_nop 1
	s_nop 1
	s_nop 1
	s_nop 1
	s_nop 1
	s_nop 1
	s_waitcnt lgkmcnt(0)
	v_and_b32_e32 v252, 0x7f, v178
	v_cmp_gt_i32_e64 s[6:7], 0, v178
	v_xor_b32_e32 v178, 0x7f, v252
	s_nop 0
	v_cndmask_b32_e64 v173, v178, v252, s[6:7]
	v_lshl_add_u32 v252, v8, 8, v207
	ds_read_b32 v178, v252 offset:4096
	s_nop 1
	s_nop 1
	s_nop 1
	s_nop 1
	s_nop 1
	s_nop 1
	s_nop 1
	s_nop 1
	s_nop 1
	s_nop 1
	s_nop 1
	s_nop 1
	s_nop 1
	s_nop 1
	s_nop 1
	s_nop 1
	s_waitcnt lgkmcnt(0)
	v_and_b32_e32 v252, 0x7f, v178
	v_cmp_gt_i32_e64 s[6:7], 0, v178
	v_xor_b32_e32 v178, 0x7f, v252
	s_nop 0
	v_cndmask_b32_e64 v8, v178, v252, s[6:7]
	v_lshl_add_u32 v8, v173, 7, v8
	v_min_f32_e32 v15, v14, v62
	v_and_b32_e32 v173, 0xff, v15
	v_bitop3_b32 v178, v15, s10, v15 bitop3:0xc
	v_cmp_gt_i32_e64 s[8:9], 0, v15
	v_and_b32_e32 v63, 0xffffff00, v15
	v_max_f32_e32 v14, v14, v62
	v_cndmask_b32_e64 v15, v178, v173, s[8:9]
	v_lshrrev_b32_e32 v173, 4, v15
	v_lshl_add_u32 v252, v173, 8, v207
	ds_read_b32 v178, v252
	v_and_b32_e32 v15, 15, v15
	v_cmp_gt_i32_e64 s[6:7], 0, v14
	v_and_b32_e32 v62, 0xffffff00, v14
	s_nop 0
	s_nop 1
	s_nop 1
	s_nop 1
	s_nop 1
	s_nop 1
	s_nop 1
	s_nop 1
	s_nop 1
	s_nop 1
	s_nop 1
	s_nop 1
	s_nop 1
	s_nop 1
	s_nop 1
	s_waitcnt lgkmcnt(0)
	v_and_b32_e32 v252, 0x7f, v178
	v_cmp_gt_i32_e64 s[8:9], 0, v178
	v_xor_b32_e32 v178, 0x7f, v252
	s_nop 0
	v_cndmask_b32_e64 v173, v178, v252, s[8:9]
	v_lshl_add_u32 v252, v15, 8, v207
	ds_read_b32 v178, v252 offset:4096
	s_nop 1
	s_nop 1
	s_nop 1
	s_nop 1
	s_nop 1
	s_nop 1
	s_nop 1
	s_nop 1
	s_nop 1
	s_nop 1
	s_nop 1
	s_nop 1
	s_nop 1
	s_nop 1
	s_nop 1
	s_nop 1
	s_waitcnt lgkmcnt(0)
	v_and_b32_e32 v252, 0x7f, v178
	v_cmp_gt_i32_e64 s[8:9], 0, v178
	v_xor_b32_e32 v178, 0x7f, v252
	s_nop 0
	v_cndmask_b32_e64 v15, v178, v252, s[8:9]
	v_lshl_add_u32 v15, v173, 7, v15
	v_and_b32_e32 v173, 0xff, v14
	v_bitop3_b32 v178, v14, s10, v14 bitop3:0xc
	v_cndmask_b32_e64 v14, v178, v173, s[6:7]
	v_lshrrev_b32_e32 v173, 4, v14
	v_lshl_add_u32 v252, v173, 8, v207
	ds_read_b32 v178, v252
	v_and_b32_e32 v14, 15, v14
	v_readlane_b32 s8, v253, 23
	v_readlane_b32 s9, v253, 24
	s_nop 0
	s_nop 1
	s_nop 1
	s_nop 1
	s_nop 1
	s_nop 1
	s_nop 1
	s_nop 1
	s_nop 1
	s_nop 1
	s_nop 1
	s_nop 1
	s_nop 1
	s_nop 1
	s_nop 1
	s_waitcnt lgkmcnt(0)
	v_and_b32_e32 v252, 0x7f, v178
	v_cmp_gt_i32_e64 s[6:7], 0, v178
	v_xor_b32_e32 v178, 0x7f, v252
	s_nop 0
	v_cndmask_b32_e64 v173, v178, v252, s[6:7]
	v_lshl_add_u32 v252, v14, 8, v207
	ds_read_b32 v178, v252 offset:4096
	s_nop 1
	s_nop 1
	s_nop 1
	s_nop 1
	s_nop 1
	s_nop 1
	s_nop 1
	s_nop 1
	s_nop 1
	s_nop 1
	s_nop 1
	s_nop 1
	s_nop 1
	s_nop 1
	s_nop 1
	s_nop 1
	s_waitcnt lgkmcnt(0)
	v_and_b32_e32 v252, 0x7f, v178
	v_cmp_gt_i32_e64 s[6:7], 0, v178
	v_xor_b32_e32 v178, 0x7f, v252
	s_nop 0
	v_cndmask_b32_e64 v14, v178, v252, s[6:7]
	v_lshl_add_u32 v14, v173, 7, v14
	v_and_b32_e32 v173, 0xff, v13
	v_bitop3_b32 v178, v13, s10, v13 bitop3:0xc
	v_cmp_gt_i32_e64 s[6:7], 0, v13
	s_nop 1
	v_cndmask_b32_e64 v13, v178, v173, s[6:7]
	v_lshrrev_b32_e32 v173, 4, v13
	v_lshl_add_u32 v252, v173, 8, v207
	ds_read_b32 v178, v252
	v_and_b32_e32 v13, 15, v13
	s_nop 0
	s_nop 1
	s_nop 1
	s_nop 1
	s_nop 1
	s_nop 1
	s_nop 1
	s_nop 1
	s_nop 1
	s_nop 1
	s_nop 1
	s_nop 1
	s_nop 1
	s_nop 1
	s_nop 1
	s_nop 1
	s_waitcnt lgkmcnt(0)
	v_and_b32_e32 v252, 0x7f, v178
	v_cmp_gt_i32_e64 s[6:7], 0, v178
	v_xor_b32_e32 v178, 0x7f, v252
	s_nop 0
	v_cndmask_b32_e64 v173, v178, v252, s[6:7]
	v_lshl_add_u32 v252, v13, 8, v207
	ds_read_b32 v178, v252 offset:4096
	s_nop 1
	s_nop 1
	s_nop 1
	s_nop 1
	s_nop 1
	s_nop 1
	s_nop 1
	s_nop 1
	s_nop 1
	s_nop 1
	s_nop 1
	s_nop 1
	s_nop 1
	s_nop 1
	s_nop 1
	s_nop 1
	s_waitcnt lgkmcnt(0)
	v_and_b32_e32 v252, 0x7f, v178
	v_cmp_gt_i32_e64 s[6:7], 0, v178
	v_xor_b32_e32 v178, 0x7f, v252
	s_nop 0
	v_cndmask_b32_e64 v13, v178, v252, s[6:7]
	v_lshl_add_u32 v13, v173, 7, v13
	v_and_b32_e32 v173, 0xff, v59
	v_bitop3_b32 v178, v59, s10, v59 bitop3:0xc
	v_cndmask_b32_e32 v59, v178, v173, vcc
	v_lshrrev_b32_e32 v173, 4, v59
	v_cmp_gt_u32_e32 vcc, 16, v59
	s_nop 1
	v_cndmask_b32_e32 v49, 0, v49, vcc
	v_cmp_eq_u32_e32 vcc, 1, v173
	s_nop 1
	v_cndmask_b32_e32 v48, v49, v48, vcc
	v_cmp_eq_u32_e32 vcc, 2, v173
	s_nop 1
	v_cndmask_b32_e32 v47, v48, v47, vcc
	v_cmp_eq_u32_e32 vcc, 3, v173
	s_nop 1
	v_cndmask_b32_e32 v46, v47, v46, vcc
	v_cmp_eq_u32_e32 vcc, 4, v173
	s_nop 1
	v_cndmask_b32_e32 v45, v46, v45, vcc
	v_cmp_eq_u32_e32 vcc, 5, v173
	s_nop 1
	v_cndmask_b32_e32 v44, v45, v44, vcc
	v_cmp_eq_u32_e32 vcc, 6, v173
	s_nop 1
	v_cndmask_b32_e32 v43, v44, v43, vcc
	v_cmp_eq_u32_e32 vcc, 7, v173
	s_nop 1
	v_cndmask_b32_e32 v42, v43, v42, vcc
	v_cmp_eq_u32_e32 vcc, 8, v173
	s_nop 1
	v_cndmask_b32_e32 v41, v42, v41, vcc
	v_cmp_eq_u32_e32 vcc, 9, v173
	s_nop 1
	v_cndmask_b32_e32 v40, v41, v40, vcc
	v_cmp_eq_u32_e32 vcc, 10, v173
	s_nop 1
	v_cndmask_b32_e32 v39, v40, v39, vcc
	v_cmp_eq_u32_e32 vcc, 11, v173
	s_nop 1
	v_cndmask_b32_e32 v38, v39, v38, vcc
	v_cmp_eq_u32_e32 vcc, 12, v173
	v_and_b32_e32 v39, 15, v59
	s_nop 0
	v_cndmask_b32_e32 v37, v38, v37, vcc
	v_cmp_eq_u32_e32 vcc, 13, v173
	s_nop 1
	v_cndmask_b32_e32 v36, v37, v36, vcc
	v_cmp_eq_u32_e32 vcc, 14, v173
	s_nop 1
	v_cndmask_b32_e32 v35, v36, v35, vcc
	v_cmp_eq_u32_e32 vcc, 15, v173
	v_exp_f32_e32 v36, v12
	v_and_b32_e32 v12, 0xffffff00, v32
	v_cndmask_b32_e32 v38, v35, v34, vcc
	v_cmp_eq_u32_e32 vcc, 0, v39
	v_sub_f32_e32 v12, v12, v60
	v_mul_f32_e32 v12, 0x3fb8aa3b, v12
	v_cndmask_b32_e32 v33, 0, v33, vcc
	v_cmp_eq_u32_e32 vcc, 1, v39
	v_exp_f32_e32 v37, v12
	s_nop 0
	v_cndmask_b32_e32 v17, v33, v17, vcc
	v_cmp_eq_u32_e32 vcc, 2, v39
	v_sub_f32_e32 v33, v51, v60
	v_mul_f32_e32 v33, 0x3fb8aa3b, v33
	v_cndmask_b32_e32 v17, v17, v18, vcc
	v_cmp_eq_u32_e32 vcc, 3, v39
	v_sub_f32_e32 v18, v60, v60
	v_mul_f32_e32 v18, 0x3fb8aa3b, v18
	v_cndmask_b32_e32 v17, v17, v19, vcc
	v_cmp_eq_u32_e32 vcc, 4, v39
	v_sub_f32_e32 v19, v61, v60
	v_exp_f32_e32 v18, v18
	v_cndmask_b32_e32 v17, v17, v20, vcc
	v_cmp_eq_u32_e32 vcc, 5, v39
	v_mul_f32_e32 v19, 0x3fb8aa3b, v19
	v_sub_f32_e32 v20, v62, v60
	v_cndmask_b32_e32 v17, v17, v21, vcc
	v_exp_f32_e32 v19, v19
	v_mul_f32_e32 v20, 0x3fb8aa3b, v20
	v_sub_f32_e32 v21, v63, v60
	v_cmp_eq_u32_e32 vcc, 6, v39
	v_exp_f32_e32 v20, v20
	v_mul_f32_e32 v21, 0x3fb8aa3b, v21
	v_cndmask_b32_e32 v17, v17, v22, vcc
	v_cmp_eq_u32_e32 vcc, 7, v39
	v_exp_f32_e32 v21, v21
	v_add_f32_e32 v22, 0, v18
	v_cndmask_b32_e32 v17, v17, v23, vcc
	v_cmp_eq_u32_e32 vcc, 8, v39
	v_add_f32_e32 v22, v19, v22
	v_add_f32_e32 v22, v20, v22
	v_cndmask_b32_e32 v17, v17, v24, vcc
	v_cmp_eq_u32_e32 vcc, 9, v39
	v_sub_f32_e32 v23, v56, v60
	v_mul_f32_e32 v23, 0x3fb8aa3b, v23
	v_cndmask_b32_e32 v17, v17, v25, vcc
	v_cmp_eq_u32_e32 vcc, 10, v39
	v_sub_f32_e32 v24, v55, v60
	v_exp_f32_e32 v23, v23
	v_cndmask_b32_e32 v17, v17, v26, vcc
	v_add_f32_e32 v26, v21, v22
	v_sub_f32_e32 v22, v58, v60
	v_mul_f32_e32 v22, 0x3fb8aa3b, v22
	v_exp_f32_e32 v22, v22
	v_mul_f32_e32 v24, 0x3fb8aa3b, v24
	v_sub_f32_e32 v25, v54, v60
	v_exp_f32_e32 v24, v24
	v_mul_f32_e32 v25, 0x3fb8aa3b, v25
	v_cmp_eq_u32_e32 vcc, 11, v39
	v_exp_f32_e32 v25, v25
	v_add_f32_e32 v26, v22, v26
	v_cndmask_b32_e32 v17, v17, v27, vcc
	v_cmp_eq_u32_e32 vcc, 12, v39
	v_add_f32_e32 v26, v23, v26
	v_add_f32_e32 v26, v24, v26
	v_cndmask_b32_e32 v17, v17, v28, vcc
	v_cmp_eq_u32_e32 vcc, 13, v39
	v_sub_f32_e32 v27, v57, v60
	v_mul_f32_e32 v27, 0x3fb8aa3b, v27
	v_cndmask_b32_e32 v17, v17, v29, vcc
	v_cmp_eq_u32_e32 vcc, 14, v39
	v_sub_f32_e32 v28, v53, v60
	v_exp_f32_e32 v27, v27
	v_cndmask_b32_e32 v17, v17, v30, vcc
	v_add_f32_e32 v30, v25, v26
	v_sub_f32_e32 v26, v209, v60
	v_mul_f32_e32 v26, 0x3fb8aa3b, v26
	v_exp_f32_e32 v26, v26
	v_mul_f32_e32 v28, 0x3fb8aa3b, v28
	v_sub_f32_e32 v29, v52, v60
	v_exp_f32_e32 v28, v28
	v_mul_f32_e32 v29, 0x3fb8aa3b, v29
	v_exp_f32_e32 v29, v29
	v_exp_f32_e32 v34, v33
	v_sub_f32_e32 v33, v50, v60
	v_add_f32_e32 v30, v26, v30
	v_mul_f32_e32 v33, 0x3fb8aa3b, v33
	v_add_f32_e32 v30, v27, v30
	v_exp_f32_e32 v35, v33
	v_add_f32_e32 v30, v28, v30
	v_add_f32_e32 v30, v29, v30
	v_add_f32_e32 v12, v34, v30
	v_add_f32_e32 v12, v35, v12
	v_add_f32_e32 v12, v36, v12
	v_add_f32_e32 v30, v37, v12
	v_div_scale_f32 v32, s[6:7], v30, v30, 1.0
	v_rcp_f32_e32 v33, v32
	v_cmp_eq_u32_e32 vcc, 15, v39
	v_readlane_b32 s6, v255, 46
	s_lshl_b32 s6, s6, 4
	v_cndmask_b32_e32 v12, v17, v31, vcc
	v_fma_f32 v17, -v32, v33, 1.0
	v_fmac_f32_e32 v33, v17, v33
	v_div_scale_f32 v17, vcc, 1.0, v30, 1.0
	v_mul_f32_e32 v31, v17, v33
	v_lshl_add_u32 v12, v38, 7, v12
	v_fma_f32 v38, -v32, v31, v17
	v_fmac_f32_e32 v31, v38, v33
	v_fma_f32 v17, -v32, v31, v17
	v_div_fmas_f32 v17, v17, v33, v31
	v_div_fixup_f32 v30, v17, v30, 1.0
	v_lshlrev_b64 v[16:17], 9, v[176:177]
	s_ashr_i32 s7, s6, 31
	v_lshl_add_u64 v[32:33], s[94:95], 0, v[16:17]
	s_lshl_b64 s[6:7], s[6:7], 2
	v_lshl_add_u64 v[32:33], v[32:33], 0, s[6:7]
	v_lshl_add_u64 v[16:17], s[8:9], 0, v[16:17]
	v_lshl_add_u64 v[16:17], v[16:17], 0, s[6:7]
	global_store_dwordx4 v[32:33], v[12:15], off
	v_readlane_b32 s8, v255, 44
	v_readlane_b32 s9, v255, 45
	v_pk_mul_f32 v[12:13], v[18:19], v[30:31] op_sel_hi:[1,0]
	v_pk_mul_f32 v[14:15], v[20:21], v[30:31] op_sel_hi:[1,0]
	global_store_dwordx4 v[16:17], v[12:15], off
	global_store_dwordx4 v[32:33], v[8:11], off offset:16
	s_nop 1
	v_pk_mul_f32 v[8:9], v[22:23], v[30:31] op_sel_hi:[1,0]
	v_pk_mul_f32 v[10:11], v[24:25], v[30:31] op_sel_hi:[1,0]
	global_store_dwordx4 v[16:17], v[8:11], off offset:16
	global_store_dwordx4 v[32:33], v[4:7], off offset:32
	s_nop 1
	v_pk_mul_f32 v[4:5], v[26:27], v[30:31] op_sel_hi:[1,0]
	v_pk_mul_f32 v[6:7], v[28:29], v[30:31] op_sel_hi:[1,0]
	global_store_dwordx4 v[16:17], v[4:7], off offset:32
	global_store_dwordx4 v[32:33], v[0:3], off offset:48
	s_nop 1
	v_pk_mul_f32 v[0:1], v[34:35], v[30:31] op_sel_hi:[1,0]
	v_pk_mul_f32 v[2:3], v[36:37], v[30:31] op_sel_hi:[1,0]
	global_store_dwordx4 v[16:17], v[0:3], off offset:48
	s_branch .LBB0_696
